# speedup vs baseline: 1.0354x; 1.0179x over previous
.LBB0_18:
	s_or_b64 exec, exec, s[0:1]
	v_ashrrev_i32_e32 v19, 31, v18
	v_lshlrev_b64 v[24:25], 5, v[18:19]
	v_lshl_add_u64 v[20:21], v[20:21], 0, v[24:25]
	global_load_dwordx4 v[24:27], v[20:21], off offset:16 nt
	global_load_dwordx4 v[28:31], v[20:21], off nt
	v_ashrrev_i32_e32 v11, 7, v14
	v_ashrrev_i32_e32 v19, 7, v18
	s_waitcnt vmcnt(3)
	v_cvt_pk_f16_f32 v7, v6, v7
	v_cvt_pk_f16_f32 v6, v4, v5
	s_waitcnt vmcnt(2)
	v_cvt_pk_f16_f32 v4, v0, v1
	v_add_u32_e32 v0, v11, v23
	v_cvt_pk_f16_f32 v5, v2, v3
	v_add_u32_e32 v2, v19, v22
	v_ashrrev_i32_e32 v1, 31, v0
	v_bfe_u32 v20, v18, 3, 4
	v_ashrrev_i32_e32 v3, 31, v2
	v_mad_u64_u32 v[0:1], s[0:1], v12, v13, v[0:1]
	v_and_b32_e32 v14, 7, v14
	v_mad_u64_u32 v[2:3], s[0:1], v10, v20, v[2:3]
	v_lshlrev_b64 v[0:1], 7, v[0:1]
	v_and_b32_e32 v18, 7, v18
	v_mov_b32_e32 v15, 0
	v_lshlrev_b32_e32 v14, 4, v14
	v_lshlrev_b64 v[2:3], 7, v[2:3]
	v_lshl_add_u64 v[0:1], v[8:9], 0, v[0:1]
	v_lshl_add_u64 v[8:9], v[16:17], 0, v[2:3]
	v_lshl_add_u64 v[0:1], v[0:1], 0, v[14:15]
	v_lshlrev_b32_e32 v14, 4, v18
	global_store_dwordx4 v[0:1], v[4:7], off sc1
	s_waitcnt vmcnt(2)
	v_cvt_pk_f16_f32 v3, v26, v27
	v_cvt_pk_f16_f32 v2, v24, v25
	s_waitcnt vmcnt(1)
	v_cvt_pk_f16_f32 v1, v30, v31
	v_cvt_pk_f16_f32 v0, v28, v29
	v_lshl_add_u64 v[4:5], v[8:9], 0, v[14:15]
	global_store_dwordx4 v[4:5], v[0:3], off sc1
	s_endpgm
	.p2align	8

.LBB1_94:
	s_or_b64 exec, exec, s[6:7]
	s_lshl_b32 s4, s28, 1
	s_add_u32 s6, s14, s4
	s_addc_u32 s7, s15, 0
	s_lshl_b64 s[4:5], s[36:37], 1
	s_add_u32 s4, s6, s4
	s_addc_u32 s5, s7, s5
	s_add_u32 s6, s38, s30
	s_addc_u32 s7, s39, 0
	s_lshl_b64 s[6:7], s[6:7], 7
	s_add_u32 s6, s16, s6
	s_addc_u32 s7, s17, s7
	s_waitcnt vmcnt(0)
	v_lshlrev_b32_e32 v6, 3, v13
	v_mov_b32_e32 v7, 0
	v_lshl_add_u64 v[14:15], s[6:7], 0, v[6:7]
	v_lshlrev_b32_e32 v6, 3, v11
	s_waitcnt lgkmcnt(0)
	v_lshl_add_u64 v[20:21], v[14:15], 0, v[6:7]
	global_load_dwordx2 v[24:25], v[20:21], off sc1
	global_load_dwordx2 v[26:27], v[20:21], off offset:8 sc1
	v_lshl_add_u32 v6, v1, 2, s64
	ds_read_b128 v[20:23], v19
	v_add_u32_e32 v40, 0xc000, v6
	ds_read2_b32 v[28:29], v40 offset1:32
	v_lshlrev_b32_e32 v6, 3, v9
	v_lshl_add_u64 v[30:31], v[14:15], 0, v[6:7]
	s_waitcnt lgkmcnt(1)
	v_cvt_f32_f16_e32 v32, v20
	v_cvt_f32_f16_sdwa v33, v20 dst_sel:DWORD dst_unused:UNUSED_PAD src0_sel:WORD_1
	v_cvt_f32_f16_e32 v20, v21
	v_cvt_f32_f16_sdwa v21, v21 dst_sel:DWORD dst_unused:UNUSED_PAD src0_sel:WORD_1
	v_cvt_f32_f16_e32 v34, v22
	v_cvt_f32_f16_sdwa v35, v22 dst_sel:DWORD dst_unused:UNUSED_PAD src0_sel:WORD_1
	v_cvt_f32_f16_e32 v22, v23
	v_cvt_f32_f16_sdwa v23, v23 dst_sel:DWORD dst_unused:UNUSED_PAD src0_sel:WORD_1
	s_waitcnt lgkmcnt(0)
	v_mov_b32_e32 v6, v29
	v_mov_b32_e32 v11, v7
	v_mov_b32_e32 v13, v7
	v_lshl_add_u64 v[10:11], s[4:5], 0, v[10:11]
	v_lshl_add_u64 v[12:13], v[10:11], 0, v[12:13]
	v_mov_b32_e32 v9, v7
	v_lshl_add_u64 v[8:9], v[10:11], 0, v[8:9]
	s_waitcnt vmcnt(1)
	v_cvt_f32_f16_e32 v36, v24
	v_cvt_f32_f16_sdwa v37, v24 dst_sel:DWORD dst_unused:UNUSED_PAD src0_sel:WORD_1
	v_cvt_f32_f16_e32 v24, v25
	v_cvt_f32_f16_sdwa v25, v25 dst_sel:DWORD dst_unused:UNUSED_PAD src0_sel:WORD_1
	s_waitcnt vmcnt(0)
	v_cvt_f32_f16_e32 v38, v26
	v_cvt_f32_f16_sdwa v39, v26 dst_sel:DWORD dst_unused:UNUSED_PAD src0_sel:WORD_1
	v_cvt_f32_f16_e32 v26, v27
	v_cvt_f32_f16_sdwa v27, v27 dst_sel:DWORD dst_unused:UNUSED_PAD src0_sel:WORD_1
	v_pk_mul_f32 v[36:37], v[6:7], v[36:37] op_sel_hi:[0,1]
	v_pk_mul_f32 v[24:25], v[6:7], v[24:25] op_sel_hi:[0,1]
	v_pk_mul_f32 v[38:39], v[6:7], v[38:39] op_sel_hi:[0,1]
	v_pk_mul_f32 v[26:27], v[6:7], v[26:27] op_sel_hi:[0,1]
	v_pk_fma_f32 v[32:33], v[28:29], v[32:33], v[36:37] op_sel_hi:[0,1,1]
	v_pk_fma_f32 v[24:25], v[28:29], v[20:21], v[24:25] op_sel_hi:[0,1,1]
	v_pk_fma_f32 v[34:35], v[28:29], v[34:35], v[38:39] op_sel_hi:[0,1,1]
	v_pk_fma_f32 v[26:27], v[28:29], v[22:23], v[26:27] op_sel_hi:[0,1,1]
	v_cvt_pk_f16_f32 v20, v32, v33
	v_cvt_pk_f16_f32 v21, v24, v25
	v_cvt_pk_f16_f32 v22, v34, v35
	v_cvt_pk_f16_f32 v23, v26, v27
	global_store_dwordx4 v[12:13], v[20:23], off sc1
	global_load_dwordx2 v[12:13], v[30:31], off sc1
	s_nop 0
	global_load_dwordx2 v[22:23], v[30:31], off offset:8 sc1
	ds_read_b128 v[18:21], v18
	ds_read2_b32 v[24:25], v40 offset0:8 offset1:40
	v_lshlrev_b32_e32 v6, 3, v5
	v_lshl_add_u64 v[26:27], v[14:15], 0, v[6:7]
	v_mov_b32_e32 v5, v7
	s_waitcnt lgkmcnt(1)
	v_cvt_f32_f16_e32 v28, v18
	v_cvt_f32_f16_sdwa v29, v18 dst_sel:DWORD dst_unused:UNUSED_PAD src0_sel:WORD_1
	v_cvt_f32_f16_e32 v18, v19
	v_cvt_f32_f16_sdwa v19, v19 dst_sel:DWORD dst_unused:UNUSED_PAD src0_sel:WORD_1
	v_cvt_f32_f16_e32 v30, v20
	v_cvt_f32_f16_sdwa v31, v20 dst_sel:DWORD dst_unused:UNUSED_PAD src0_sel:WORD_1
	v_cvt_f32_f16_e32 v20, v21
	v_cvt_f32_f16_sdwa v21, v21 dst_sel:DWORD dst_unused:UNUSED_PAD src0_sel:WORD_1
	s_waitcnt lgkmcnt(0)
	v_mov_b32_e32 v6, v25
	v_lshl_add_u64 v[4:5], v[10:11], 0, v[4:5]
	s_waitcnt vmcnt(1)
	v_cvt_f32_f16_e32 v32, v12
	v_cvt_f32_f16_sdwa v33, v12 dst_sel:DWORD dst_unused:UNUSED_PAD src0_sel:WORD_1
	v_cvt_f32_f16_e32 v12, v13
	v_cvt_f32_f16_sdwa v13, v13 dst_sel:DWORD dst_unused:UNUSED_PAD src0_sel:WORD_1
	s_waitcnt vmcnt(0)
	v_cvt_f32_f16_e32 v34, v22
	v_cvt_f32_f16_sdwa v35, v22 dst_sel:DWORD dst_unused:UNUSED_PAD src0_sel:WORD_1
	v_cvt_f32_f16_e32 v22, v23
	v_cvt_f32_f16_sdwa v23, v23 dst_sel:DWORD dst_unused:UNUSED_PAD src0_sel:WORD_1
	v_pk_mul_f32 v[32:33], v[6:7], v[32:33] op_sel_hi:[0,1]
	v_pk_mul_f32 v[12:13], v[6:7], v[12:13] op_sel_hi:[0,1]
	v_pk_mul_f32 v[34:35], v[6:7], v[34:35] op_sel_hi:[0,1]
	v_pk_mul_f32 v[22:23], v[6:7], v[22:23] op_sel_hi:[0,1]
	v_pk_fma_f32 v[28:29], v[24:25], v[28:29], v[32:33] op_sel_hi:[0,1,1]
	v_pk_fma_f32 v[12:13], v[24:25], v[18:19], v[12:13] op_sel_hi:[0,1,1]
	v_pk_fma_f32 v[30:31], v[24:25], v[30:31], v[34:35] op_sel_hi:[0,1,1]
	v_pk_fma_f32 v[22:23], v[24:25], v[20:21], v[22:23] op_sel_hi:[0,1,1]
	v_cvt_pk_f16_f32 v18, v28, v29
	v_cvt_pk_f16_f32 v19, v12, v13
	v_cvt_pk_f16_f32 v20, v30, v31
	v_cvt_pk_f16_f32 v21, v22, v23
	global_store_dwordx4 v[8:9], v[18:21], off sc1
	global_load_dwordx2 v[8:9], v[26:27], off sc1
	s_nop 0
	global_load_dwordx2 v[12:13], v[26:27], off offset:8 sc1
	ds_read_b128 v[18:21], v17
	ds_read2_b32 v[22:23], v40 offset0:16 offset1:48
	v_lshlrev_b32_e32 v6, 3, v3
	v_lshl_add_u64 v[24:25], v[14:15], 0, v[6:7]
	v_mov_b32_e32 v3, v7
	s_waitcnt lgkmcnt(1)
	v_cvt_f32_f16_e32 v14, v18
	v_cvt_f32_f16_sdwa v15, v18 dst_sel:DWORD dst_unused:UNUSED_PAD src0_sel:WORD_1
	v_cvt_f32_f16_e32 v18, v19
	v_cvt_f32_f16_sdwa v19, v19 dst_sel:DWORD dst_unused:UNUSED_PAD src0_sel:WORD_1
	v_cvt_f32_f16_e32 v26, v20
	v_cvt_f32_f16_sdwa v27, v20 dst_sel:DWORD dst_unused:UNUSED_PAD src0_sel:WORD_1
	v_cvt_f32_f16_e32 v20, v21
	v_cvt_f32_f16_sdwa v21, v21 dst_sel:DWORD dst_unused:UNUSED_PAD src0_sel:WORD_1
	s_waitcnt lgkmcnt(0)
	v_mov_b32_e32 v6, v23
	v_lshl_add_u64 v[2:3], v[10:11], 0, v[2:3]
	s_waitcnt vmcnt(1)
	v_cvt_f32_f16_e32 v28, v8
	v_cvt_f32_f16_sdwa v29, v8 dst_sel:DWORD dst_unused:UNUSED_PAD src0_sel:WORD_1
	v_cvt_f32_f16_e32 v8, v9
	v_cvt_f32_f16_sdwa v9, v9 dst_sel:DWORD dst_unused:UNUSED_PAD src0_sel:WORD_1
	s_waitcnt vmcnt(0)
	v_cvt_f32_f16_e32 v30, v12
	v_cvt_f32_f16_sdwa v31, v12 dst_sel:DWORD dst_unused:UNUSED_PAD src0_sel:WORD_1
	v_cvt_f32_f16_e32 v12, v13
	v_cvt_f32_f16_sdwa v13, v13 dst_sel:DWORD dst_unused:UNUSED_PAD src0_sel:WORD_1
	v_pk_mul_f32 v[28:29], v[6:7], v[28:29] op_sel_hi:[0,1]
	v_pk_mul_f32 v[8:9], v[6:7], v[8:9] op_sel_hi:[0,1]
	v_pk_mul_f32 v[30:31], v[6:7], v[30:31] op_sel_hi:[0,1]
	v_pk_mul_f32 v[12:13], v[6:7], v[12:13] op_sel_hi:[0,1]
	v_pk_fma_f32 v[14:15], v[22:23], v[14:15], v[28:29] op_sel_hi:[0,1,1]
	v_pk_fma_f32 v[8:9], v[22:23], v[18:19], v[8:9] op_sel_hi:[0,1,1]
	v_pk_fma_f32 v[18:19], v[22:23], v[26:27], v[30:31] op_sel_hi:[0,1,1]
	v_pk_fma_f32 v[20:21], v[22:23], v[20:21], v[12:13] op_sel_hi:[0,1,1]
	v_cvt_pk_f16_f32 v12, v14, v15
	v_cvt_pk_f16_f32 v13, v8, v9
	v_cvt_pk_f16_f32 v14, v18, v19
	v_cvt_pk_f16_f32 v15, v20, v21
	global_store_dwordx4 v[4:5], v[12:15], off sc1
	global_load_dwordx2 v[4:5], v[24:25], off sc1
	s_nop 0
	global_load_dwordx2 v[8:9], v[24:25], off offset:8 sc1
	ds_read_b128 v[12:15], v16
	ds_read2_b32 v[16:17], v40 offset0:24 offset1:56
	s_waitcnt lgkmcnt(1)
	v_cvt_f32_f16_e32 v6, v12
	v_cvt_f32_f16_sdwa v7, v12 dst_sel:DWORD dst_unused:UNUSED_PAD src0_sel:WORD_1
	v_cvt_f32_f16_e32 v18, v13
	v_cvt_f32_f16_sdwa v19, v13 dst_sel:DWORD dst_unused:UNUSED_PAD src0_sel:WORD_1
	v_cvt_f32_f16_e32 v20, v14
	v_cvt_f32_f16_sdwa v21, v14 dst_sel:DWORD dst_unused:UNUSED_PAD src0_sel:WORD_1
	v_cvt_f32_f16_e32 v14, v15
	v_cvt_f32_f16_sdwa v15, v15 dst_sel:DWORD dst_unused:UNUSED_PAD src0_sel:WORD_1
	s_waitcnt lgkmcnt(0)
	v_mov_b32_e32 v12, v17
	s_waitcnt vmcnt(1)
	v_cvt_f32_f16_e32 v22, v4
	v_cvt_f32_f16_sdwa v23, v4 dst_sel:DWORD dst_unused:UNUSED_PAD src0_sel:WORD_1
	v_cvt_f32_f16_e32 v4, v5
	v_cvt_f32_f16_sdwa v5, v5 dst_sel:DWORD dst_unused:UNUSED_PAD src0_sel:WORD_1
	s_waitcnt vmcnt(0)
	v_cvt_f32_f16_e32 v24, v8
	v_cvt_f32_f16_sdwa v25, v8 dst_sel:DWORD dst_unused:UNUSED_PAD src0_sel:WORD_1
	v_cvt_f32_f16_e32 v8, v9
	v_cvt_f32_f16_sdwa v9, v9 dst_sel:DWORD dst_unused:UNUSED_PAD src0_sel:WORD_1
	v_pk_mul_f32 v[22:23], v[12:13], v[22:23] op_sel_hi:[0,1]
	v_pk_mul_f32 v[4:5], v[12:13], v[4:5] op_sel_hi:[0,1]
	v_pk_mul_f32 v[24:25], v[12:13], v[24:25] op_sel_hi:[0,1]
	v_pk_mul_f32 v[8:9], v[12:13], v[8:9] op_sel_hi:[0,1]
	v_pk_fma_f32 v[6:7], v[16:17], v[6:7], v[22:23] op_sel_hi:[0,1,1]
	v_pk_fma_f32 v[12:13], v[16:17], v[18:19], v[4:5] op_sel_hi:[0,1,1]
	v_pk_fma_f32 v[18:19], v[16:17], v[20:21], v[24:25] op_sel_hi:[0,1,1]
	v_pk_fma_f32 v[8:9], v[16:17], v[14:15], v[8:9] op_sel_hi:[0,1,1]
	v_cvt_pk_f16_f32 v4, v6, v7
	v_cvt_pk_f16_f32 v5, v12, v13
	v_cvt_pk_f16_f32 v6, v18, v19
	v_cvt_pk_f16_f32 v7, v8, v9
	global_store_dwordx4 v[2:3], v[4:7], off sc1

.LBB1_124:
	v_add_f32_e32 v67, v50, v51
	v_add_u32_e32 v76, s64, v213
	v_add_f32_e32 v67, v52, v67
	ds_read_b64_tr_b16 v[68:69], v76 offset:24576
	ds_read_b64_tr_b16 v[70:71], v76 offset:25088
	v_add_f32_e32 v67, v53, v67
	v_add_f32_e32 v67, v54, v67
	v_add_f32_e32 v67, v55, v67
	v_add_f32_e32 v67, v56, v67
	v_add_f32_e32 v67, v57, v67
	v_cvt_pk_f16_f32 v50, v50, v51
	v_cvt_pk_f16_f32 v51, v52, v53
	v_cvt_pk_f16_f32 v52, v54, v55
	v_cvt_pk_f16_f32 v53, v56, v57
	ds_read_b64_tr_b16 v[54:55], v76 offset:25600
	ds_read_b64_tr_b16 v[56:57], v76 offset:26112
	s_waitcnt lgkmcnt(2)
	v_mfma_f32_32x32x16_f16 v[18:33], v[50:53], v[68:71], v[18:33]
	ds_read_b64_tr_b16 v[68:69], v76 offset:28672
	ds_read_b64_tr_b16 v[70:71], v76 offset:29184
	v_add_f32_e32 v67, v58, v67
	v_add_f32_e32 v67, v59, v67
	v_add_f32_e32 v67, v60, v67
	ds_read_b64_tr_b16 v[72:73], v76 offset:29696
	ds_read_b64_tr_b16 v[74:75], v76 offset:30208
	v_cmp_gt_u32_e32 vcc, 32, v218
	s_waitcnt lgkmcnt(2)
	v_mfma_f32_32x32x16_f16 v[2:17], v[50:53], v[68:71], v[2:17]
	v_add_f32_e32 v50, v61, v67
	v_add_f32_e32 v50, v62, v50
	v_add_f32_e32 v67, v63, v50
	v_cvt_pk_f16_f32 v50, v58, v59
	v_cvt_pk_f16_f32 v51, v60, v61
	v_cvt_pk_f16_f32 v52, v62, v63
	v_cvt_pk_f16_f32 v53, v64, v65
	s_nop 0
	v_mfma_f32_32x32x16_f16 v[18:33], v[50:53], v[54:57], v[18:33]
	v_add_f32_e32 v54, v64, v67
	v_add_f32_e32 v54, v65, v54
	v_add_f32_e32 v54, v34, v54
	v_add_f32_e32 v54, v35, v54
	v_add_f32_e32 v54, v36, v54
	v_add_f32_e32 v58, v37, v54
	v_cvt_pk_f16_f32 v34, v34, v35
	s_waitcnt lgkmcnt(0)
	v_mfma_f32_32x32x16_f16 v[2:17], v[50:53], v[72:75], v[2:17]
	ds_read_b64_tr_b16 v[50:51], v76 offset:26624
	ds_read_b64_tr_b16 v[52:53], v76 offset:27136
	v_cvt_pk_f16_f32 v35, v36, v37
	v_cvt_pk_f16_f32 v36, v38, v39
	v_cvt_pk_f16_f32 v37, v40, v41
	ds_read_b64_tr_b16 v[54:55], v76 offset:27648
	ds_read_b64_tr_b16 v[56:57], v76 offset:28160
	v_add_f32_e32 v38, v38, v58
	v_add_f32_e32 v38, v39, v38
	s_waitcnt lgkmcnt(2)
	v_mfma_f32_32x32x16_f16 v[18:33], v[34:37], v[50:53], v[18:33]
	ds_read_b64_tr_b16 v[50:51], v76 offset:30720
	ds_read_b64_tr_b16 v[52:53], v76 offset:31232
	v_add_f32_e32 v38, v40, v38
	ds_read_b64_tr_b16 v[58:59], v76 offset:31744
	ds_read_b64_tr_b16 v[60:61], v76 offset:32256
	v_cvt_pk_f16_f32 v39, v48, v49
	s_waitcnt lgkmcnt(2)
	v_mfma_f32_32x32x16_f16 v[2:17], v[34:37], v[50:53], v[2:17]
	v_add_f32_e32 v34, v41, v38
	v_add_f32_e32 v34, v42, v34
	v_add_f32_e32 v34, v43, v34
	v_add_f32_e32 v34, v44, v34
	v_cvt_pk_f16_f32 v36, v42, v43
	v_cvt_pk_f16_f32 v37, v44, v45
	v_cvt_pk_f16_f32 v38, v46, v47
	v_add_f32_e32 v34, v45, v34
	v_mfma_f32_32x32x16_f16 v[18:33], v[36:39], v[54:57], v[18:33]
	v_add_f32_e32 v34, v46, v34
	v_add_f32_e32 v34, v47, v34
	v_add_f32_e32 v34, v48, v34
	v_add_f32_e32 v34, v49, v34
	v_add_f32_e32 v34, v114, v34
	v_mov_b32_e32 v35, v34
	s_nop 1
	v_permlane32_swap_b32_e32 v34, v35
	s_waitcnt lgkmcnt(0)
	v_mfma_f32_32x32x16_f16 v[2:17], v[36:39], v[58:61], v[2:17]
	s_and_saveexec_b64 s[4:5], vcc
	v_add_f32_e32 v34, v34, v35
	ds_write_b32 v212, v34 offset:49280
	s_or_b64 exec, exec, s[4:5]
	s_waitcnt lgkmcnt(0)
	ds_read_b128 v[34:37], v66 offset:49280
	ds_read_b128 v[38:41], v66 offset:49312
	s_add_u32 s6, s14, s28
	s_addc_u32 s7, s15, s29
	s_lshl_b32 s4, s23, 12
	s_waitcnt lgkmcnt(1)
	v_rcp_f32_e32 v42, v34
	v_rcp_f32_e32 v43, v35
	v_rcp_f32_e32 v44, v36
	s_add_i32 s23, s4, 0
	v_lshlrev_b32_e32 v50, 9, v201
	v_lshlrev_b32_e32 v51, 1, v199
	v_add3_u32 v50, s23, v50, v51
	v_fma_mixlo_f16 v2, v2, v42, 0
	v_rcp_f32_e32 v45, v37
	ds_write_b16 v50, v2 offset:64
	v_fma_mixlo_f16 v2, v19, v43, 0
	ds_write_b16 v50, v2 offset:128
	v_fma_mixlo_f16 v2, v3, v43, 0
	s_waitcnt lgkmcnt(2)
	v_rcp_f32_e32 v46, v38
	ds_write_b16 v50, v2 offset:192
	v_fma_mixlo_f16 v2, v20, v44, 0
	ds_write_b16 v50, v2 offset:256
	v_fma_mixlo_f16 v2, v4, v44, 0
	v_rcp_f32_e32 v47, v39
	ds_write_b16 v50, v2 offset:320
	v_fma_mixlo_f16 v2, v21, v45, 0
	ds_read_b128 v[34:37], v66 offset:49344
	ds_write_b16 v50, v2 offset:384
	v_fma_mixlo_f16 v2, v5, v45, 0
	v_rcp_f32_e32 v48, v40
	ds_write_b16 v50, v2 offset:448
	v_fma_mixlo_f16 v2, v22, v46, 0
	ds_write_b16 v50, v2 offset:1024
	v_fma_mixlo_f16 v2, v6, v46, 0
	v_rcp_f32_e32 v49, v41
	ds_write_b16 v50, v2 offset:1088
	v_fma_mixlo_f16 v2, v23, v47, 0
	ds_write_b16 v50, v2 offset:1152
	v_fma_mixlo_f16 v2, v7, v47, 0
	ds_read_b128 v[38:41], v66 offset:49376
	s_waitcnt lgkmcnt(6)
	v_rcp_f32_e32 v34, v34
	ds_write_b16 v50, v2 offset:1216
	v_fma_mixlo_f16 v2, v24, v48, 0
	ds_write_b16 v50, v2 offset:1280
	v_fma_mixlo_f16 v2, v8, v48, 0
	v_rcp_f32_e32 v35, v35
	ds_write_b16 v50, v2 offset:1344
	v_fma_mixlo_f16 v2, v25, v49, 0
	ds_write_b16 v50, v2 offset:1408
	v_fma_mixlo_f16 v2, v9, v49, 0
	v_rcp_f32_e32 v36, v36
	ds_write_b16 v50, v2 offset:1472
	v_fma_mixlo_f16 v2, v26, v34, 0
	ds_write_b16 v50, v2 offset:2048
	v_fma_mixlo_f16 v2, v10, v34, 0
	v_rcp_f32_e32 v37, v37
	ds_write_b16 v50, v2 offset:2112
	v_fma_mixlo_f16 v2, v27, v35, 0
	ds_write_b16 v50, v2 offset:2176
	v_fma_mixlo_f16 v2, v11, v35, 0
	s_waitcnt lgkmcnt(8)
	v_rcp_f32_e32 v38, v38
	ds_write_b16 v50, v2 offset:2240
	v_fma_mixlo_f16 v2, v28, v36, 0
	ds_write_b16 v50, v2 offset:2304
	v_fma_mixlo_f16 v2, v12, v36, 0
	v_rcp_f32_e32 v39, v39
	ds_write_b16 v50, v2 offset:2368
	v_fma_mixlo_f16 v2, v29, v37, 0
	ds_write_b16 v50, v2 offset:2432
	v_fma_mixlo_f16 v2, v13, v37, 0
	v_rcp_f32_e32 v40, v40
	ds_write_b16 v50, v2 offset:2496
	v_fma_mixlo_f16 v2, v30, v38, 0
	ds_write_b16 v50, v2 offset:3072
	v_fma_mixlo_f16 v2, v14, v38, 0
	v_rcp_f32_e32 v41, v41
	ds_write_b16 v50, v2 offset:3136
	v_fma_mixlo_f16 v2, v31, v39, 0
	ds_write_b16 v50, v2 offset:3200
	v_fma_mixlo_f16 v2, v15, v39, 0
	ds_write_b16 v50, v2 offset:3264
	v_fma_mixlo_f16 v2, v32, v40, 0
	ds_write_b16 v50, v2 offset:3328
	v_fma_mixlo_f16 v2, v16, v40, 0
	ds_write_b16 v50, v2 offset:3392
	v_fma_mixlo_f16 v2, v33, v41, 0
	v_fma_mixlo_f16 v18, v18, v42, 0
	ds_write_b16 v50, v2 offset:3456
	v_fma_mixlo_f16 v2, v17, v41, 0
	s_lshl_b64 s[4:5], s[30:31], 1
	ds_write_b16 v50, v18
	ds_write_b16 v50, v2 offset:3520
	s_add_u32 s4, s6, s4
	v_lshlrev_b32_e32 v2, 4, v200
	v_lshlrev_b32_e32 v20, 7, v1
	s_addc_u32 s5, s7, s5
	s_waitcnt lgkmcnt(0)
	v_mov_b32_e32 v3, 0
	v_add3_u32 v1, s23, v2, v20
	v_lshl_add_u64 v[18:19], s[4:5], 0, v[2:3]
	v_mov_b32_e32 v21, v3
	ds_read_b128 v[2:5], v1
	ds_read_b128 v[6:9], v1 offset:1024
	ds_read_b128 v[10:13], v1 offset:2048
	ds_read_b128 v[14:17], v1 offset:3072
	v_lshl_add_u64 v[18:19], v[18:19], 0, v[20:21]
	s_waitcnt lgkmcnt(3)
	global_store_dwordx4 v[18:19], v[2:5], off sc1
	s_waitcnt lgkmcnt(2)
	global_store_dwordx4 v[18:19], v[6:9], off offset:1024 sc1
	s_waitcnt lgkmcnt(1)
	global_store_dwordx4 v[18:19], v[10:13], off offset:2048 sc1
	s_waitcnt lgkmcnt(0)
	global_store_dwordx4 v[18:19], v[14:17], off offset:3072 sc1
	s_waitcnt lgkmcnt(0)
	s_barrier
	s_load_dwordx2 s[4:5], s[0:1], 0x40
	s_branch .LBB1_276

.LBB1_220:
	s_or_b64 exec, exec, s[18:19]
	s_lshl_b32 s0, s50, 1
	s_add_u32 s7, s14, s0
	s_addc_u32 s18, s15, 0
	s_lshl_b64 s[0:1], s[24:25], 1
	s_add_u32 s0, s7, s0
	s_addc_u32 s1, s18, s1
	s_add_u32 s6, s20, s6
	s_addc_u32 s7, s21, 0
	s_lshl_b64 s[6:7], s[6:7], 7
	s_add_u32 s6, s16, s6
	s_addc_u32 s7, s17, s7
	s_waitcnt vmcnt(0)
	v_lshlrev_b32_e32 v6, 3, v13
	v_mov_b32_e32 v7, 0
	v_lshl_add_u64 v[14:15], s[6:7], 0, v[6:7]
	v_lshlrev_b32_e32 v6, 3, v11
	s_waitcnt lgkmcnt(0)
	v_lshl_add_u64 v[20:21], v[14:15], 0, v[6:7]
	global_load_dwordx2 v[24:25], v[20:21], off sc1
	global_load_dwordx2 v[26:27], v[20:21], off offset:8 sc1
	v_lshl_add_u32 v6, v199, 2, s51
	ds_read_b128 v[20:23], v19
	v_add_u32_e32 v40, 0xc000, v6
	ds_read2_b32 v[28:29], v40 offset1:32
	v_lshlrev_b32_e32 v6, 3, v9
	v_lshl_add_u64 v[30:31], v[14:15], 0, v[6:7]
	s_waitcnt lgkmcnt(1)
	v_cvt_f32_f16_e32 v32, v20
	v_cvt_f32_f16_sdwa v33, v20 dst_sel:DWORD dst_unused:UNUSED_PAD src0_sel:WORD_1
	v_cvt_f32_f16_e32 v20, v21
	v_cvt_f32_f16_sdwa v21, v21 dst_sel:DWORD dst_unused:UNUSED_PAD src0_sel:WORD_1
	v_cvt_f32_f16_e32 v34, v22
	v_cvt_f32_f16_sdwa v35, v22 dst_sel:DWORD dst_unused:UNUSED_PAD src0_sel:WORD_1
	v_cvt_f32_f16_e32 v22, v23
	v_cvt_f32_f16_sdwa v23, v23 dst_sel:DWORD dst_unused:UNUSED_PAD src0_sel:WORD_1
	s_waitcnt lgkmcnt(0)
	v_mov_b32_e32 v6, v29
	v_mov_b32_e32 v11, v7
	v_mov_b32_e32 v13, v7
	v_lshl_add_u64 v[10:11], s[0:1], 0, v[10:11]
	v_lshl_add_u64 v[12:13], v[10:11], 0, v[12:13]
	v_mov_b32_e32 v9, v7
	v_lshl_add_u64 v[8:9], v[10:11], 0, v[8:9]
	s_waitcnt vmcnt(1)
	v_cvt_f32_f16_e32 v36, v24
	v_cvt_f32_f16_sdwa v37, v24 dst_sel:DWORD dst_unused:UNUSED_PAD src0_sel:WORD_1
	v_cvt_f32_f16_e32 v24, v25
	v_cvt_f32_f16_sdwa v25, v25 dst_sel:DWORD dst_unused:UNUSED_PAD src0_sel:WORD_1
	s_waitcnt vmcnt(0)
	v_cvt_f32_f16_e32 v38, v26
	v_cvt_f32_f16_sdwa v39, v26 dst_sel:DWORD dst_unused:UNUSED_PAD src0_sel:WORD_1
	v_cvt_f32_f16_e32 v26, v27
	v_cvt_f32_f16_sdwa v27, v27 dst_sel:DWORD dst_unused:UNUSED_PAD src0_sel:WORD_1
	v_pk_mul_f32 v[36:37], v[6:7], v[36:37] op_sel_hi:[0,1]
	v_pk_mul_f32 v[24:25], v[6:7], v[24:25] op_sel_hi:[0,1]
	v_pk_mul_f32 v[38:39], v[6:7], v[38:39] op_sel_hi:[0,1]
	v_pk_mul_f32 v[26:27], v[6:7], v[26:27] op_sel_hi:[0,1]
	v_pk_fma_f32 v[32:33], v[28:29], v[32:33], v[36:37] op_sel_hi:[0,1,1]
	v_pk_fma_f32 v[24:25], v[28:29], v[20:21], v[24:25] op_sel_hi:[0,1,1]
	v_pk_fma_f32 v[34:35], v[28:29], v[34:35], v[38:39] op_sel_hi:[0,1,1]
	v_pk_fma_f32 v[26:27], v[28:29], v[22:23], v[26:27] op_sel_hi:[0,1,1]
	v_cvt_pk_f16_f32 v20, v32, v33
	v_cvt_pk_f16_f32 v21, v24, v25
	v_cvt_pk_f16_f32 v22, v34, v35
	v_cvt_pk_f16_f32 v23, v26, v27
	global_store_dwordx4 v[12:13], v[20:23], off sc1
	global_load_dwordx2 v[12:13], v[30:31], off sc1
	s_nop 0
	global_load_dwordx2 v[22:23], v[30:31], off offset:8 sc1
	ds_read_b128 v[18:21], v18
	ds_read2_b32 v[24:25], v40 offset0:8 offset1:40
	v_lshlrev_b32_e32 v6, 3, v5
	v_lshl_add_u64 v[26:27], v[14:15], 0, v[6:7]
	v_mov_b32_e32 v5, v7
	s_waitcnt lgkmcnt(1)
	v_cvt_f32_f16_e32 v28, v18
	v_cvt_f32_f16_sdwa v29, v18 dst_sel:DWORD dst_unused:UNUSED_PAD src0_sel:WORD_1
	v_cvt_f32_f16_e32 v18, v19
	v_cvt_f32_f16_sdwa v19, v19 dst_sel:DWORD dst_unused:UNUSED_PAD src0_sel:WORD_1
	v_cvt_f32_f16_e32 v30, v20
	v_cvt_f32_f16_sdwa v31, v20 dst_sel:DWORD dst_unused:UNUSED_PAD src0_sel:WORD_1
	v_cvt_f32_f16_e32 v20, v21
	v_cvt_f32_f16_sdwa v21, v21 dst_sel:DWORD dst_unused:UNUSED_PAD src0_sel:WORD_1
	s_waitcnt lgkmcnt(0)
	v_mov_b32_e32 v6, v25
	v_lshl_add_u64 v[4:5], v[10:11], 0, v[4:5]
	s_waitcnt vmcnt(1)
	v_cvt_f32_f16_e32 v32, v12
	v_cvt_f32_f16_sdwa v33, v12 dst_sel:DWORD dst_unused:UNUSED_PAD src0_sel:WORD_1
	v_cvt_f32_f16_e32 v12, v13
	v_cvt_f32_f16_sdwa v13, v13 dst_sel:DWORD dst_unused:UNUSED_PAD src0_sel:WORD_1
	s_waitcnt vmcnt(0)
	v_cvt_f32_f16_e32 v34, v22
	v_cvt_f32_f16_sdwa v35, v22 dst_sel:DWORD dst_unused:UNUSED_PAD src0_sel:WORD_1
	v_cvt_f32_f16_e32 v22, v23
	v_cvt_f32_f16_sdwa v23, v23 dst_sel:DWORD dst_unused:UNUSED_PAD src0_sel:WORD_1
	v_pk_mul_f32 v[32:33], v[6:7], v[32:33] op_sel_hi:[0,1]
	v_pk_mul_f32 v[12:13], v[6:7], v[12:13] op_sel_hi:[0,1]
	v_pk_mul_f32 v[34:35], v[6:7], v[34:35] op_sel_hi:[0,1]
	v_pk_mul_f32 v[22:23], v[6:7], v[22:23] op_sel_hi:[0,1]
	v_pk_fma_f32 v[28:29], v[24:25], v[28:29], v[32:33] op_sel_hi:[0,1,1]
	v_pk_fma_f32 v[12:13], v[24:25], v[18:19], v[12:13] op_sel_hi:[0,1,1]
	v_pk_fma_f32 v[30:31], v[24:25], v[30:31], v[34:35] op_sel_hi:[0,1,1]
	v_pk_fma_f32 v[22:23], v[24:25], v[20:21], v[22:23] op_sel_hi:[0,1,1]
	v_cvt_pk_f16_f32 v18, v28, v29
	v_cvt_pk_f16_f32 v19, v12, v13
	v_cvt_pk_f16_f32 v20, v30, v31
	v_cvt_pk_f16_f32 v21, v22, v23
	global_store_dwordx4 v[8:9], v[18:21], off sc1
	global_load_dwordx2 v[8:9], v[26:27], off sc1
	s_nop 0
	global_load_dwordx2 v[12:13], v[26:27], off offset:8 sc1
	ds_read_b128 v[18:21], v17
	ds_read2_b32 v[22:23], v40 offset0:16 offset1:48
	v_lshlrev_b32_e32 v6, 3, v3
	v_lshl_add_u64 v[24:25], v[14:15], 0, v[6:7]
	v_mov_b32_e32 v3, v7
	s_waitcnt lgkmcnt(1)
	v_cvt_f32_f16_e32 v14, v18
	v_cvt_f32_f16_sdwa v15, v18 dst_sel:DWORD dst_unused:UNUSED_PAD src0_sel:WORD_1
	v_cvt_f32_f16_e32 v18, v19
	v_cvt_f32_f16_sdwa v19, v19 dst_sel:DWORD dst_unused:UNUSED_PAD src0_sel:WORD_1
	v_cvt_f32_f16_e32 v26, v20
	v_cvt_f32_f16_sdwa v27, v20 dst_sel:DWORD dst_unused:UNUSED_PAD src0_sel:WORD_1
	v_cvt_f32_f16_e32 v20, v21
	v_cvt_f32_f16_sdwa v21, v21 dst_sel:DWORD dst_unused:UNUSED_PAD src0_sel:WORD_1
	s_waitcnt lgkmcnt(0)
	v_mov_b32_e32 v6, v23
	v_lshl_add_u64 v[2:3], v[10:11], 0, v[2:3]
	s_waitcnt vmcnt(1)
	v_cvt_f32_f16_e32 v28, v8
	v_cvt_f32_f16_sdwa v29, v8 dst_sel:DWORD dst_unused:UNUSED_PAD src0_sel:WORD_1
	v_cvt_f32_f16_e32 v8, v9
	v_cvt_f32_f16_sdwa v9, v9 dst_sel:DWORD dst_unused:UNUSED_PAD src0_sel:WORD_1
	s_waitcnt vmcnt(0)
	v_cvt_f32_f16_e32 v30, v12
	v_cvt_f32_f16_sdwa v31, v12 dst_sel:DWORD dst_unused:UNUSED_PAD src0_sel:WORD_1
	v_cvt_f32_f16_e32 v12, v13
	v_cvt_f32_f16_sdwa v13, v13 dst_sel:DWORD dst_unused:UNUSED_PAD src0_sel:WORD_1
	v_pk_mul_f32 v[28:29], v[6:7], v[28:29] op_sel_hi:[0,1]
	v_pk_mul_f32 v[8:9], v[6:7], v[8:9] op_sel_hi:[0,1]
	v_pk_mul_f32 v[30:31], v[6:7], v[30:31] op_sel_hi:[0,1]
	v_pk_mul_f32 v[12:13], v[6:7], v[12:13] op_sel_hi:[0,1]
	v_pk_fma_f32 v[14:15], v[22:23], v[14:15], v[28:29] op_sel_hi:[0,1,1]
	v_pk_fma_f32 v[8:9], v[22:23], v[18:19], v[8:9] op_sel_hi:[0,1,1]
	v_pk_fma_f32 v[18:19], v[22:23], v[26:27], v[30:31] op_sel_hi:[0,1,1]
	v_pk_fma_f32 v[20:21], v[22:23], v[20:21], v[12:13] op_sel_hi:[0,1,1]
	v_cvt_pk_f16_f32 v12, v14, v15
	v_cvt_pk_f16_f32 v13, v8, v9
	v_cvt_pk_f16_f32 v14, v18, v19
	v_cvt_pk_f16_f32 v15, v20, v21
	global_store_dwordx4 v[4:5], v[12:15], off sc1
	global_load_dwordx2 v[4:5], v[24:25], off sc1
	s_nop 0
	global_load_dwordx2 v[8:9], v[24:25], off offset:8 sc1
	ds_read_b128 v[12:15], v16
	ds_read2_b32 v[16:17], v40 offset0:24 offset1:56
	s_waitcnt lgkmcnt(1)
	v_cvt_f32_f16_e32 v6, v12
	v_cvt_f32_f16_sdwa v7, v12 dst_sel:DWORD dst_unused:UNUSED_PAD src0_sel:WORD_1
	v_cvt_f32_f16_e32 v18, v13
	v_cvt_f32_f16_sdwa v19, v13 dst_sel:DWORD dst_unused:UNUSED_PAD src0_sel:WORD_1
	v_cvt_f32_f16_e32 v20, v14
	v_cvt_f32_f16_sdwa v21, v14 dst_sel:DWORD dst_unused:UNUSED_PAD src0_sel:WORD_1
	v_cvt_f32_f16_e32 v14, v15
	v_cvt_f32_f16_sdwa v15, v15 dst_sel:DWORD dst_unused:UNUSED_PAD src0_sel:WORD_1
	s_waitcnt lgkmcnt(0)
	v_mov_b32_e32 v12, v17
	s_waitcnt vmcnt(1)
	v_cvt_f32_f16_e32 v22, v4
	v_cvt_f32_f16_sdwa v23, v4 dst_sel:DWORD dst_unused:UNUSED_PAD src0_sel:WORD_1
	v_cvt_f32_f16_e32 v4, v5
	v_cvt_f32_f16_sdwa v5, v5 dst_sel:DWORD dst_unused:UNUSED_PAD src0_sel:WORD_1
	s_waitcnt vmcnt(0)
	v_cvt_f32_f16_e32 v24, v8
	v_cvt_f32_f16_sdwa v25, v8 dst_sel:DWORD dst_unused:UNUSED_PAD src0_sel:WORD_1
	v_cvt_f32_f16_e32 v8, v9
	v_cvt_f32_f16_sdwa v9, v9 dst_sel:DWORD dst_unused:UNUSED_PAD src0_sel:WORD_1
	v_pk_mul_f32 v[22:23], v[12:13], v[22:23] op_sel_hi:[0,1]
	v_pk_mul_f32 v[4:5], v[12:13], v[4:5] op_sel_hi:[0,1]
	v_pk_mul_f32 v[24:25], v[12:13], v[24:25] op_sel_hi:[0,1]
	v_pk_mul_f32 v[8:9], v[12:13], v[8:9] op_sel_hi:[0,1]
	v_pk_fma_f32 v[6:7], v[16:17], v[6:7], v[22:23] op_sel_hi:[0,1,1]
	v_pk_fma_f32 v[12:13], v[16:17], v[18:19], v[4:5] op_sel_hi:[0,1,1]
	v_pk_fma_f32 v[18:19], v[16:17], v[20:21], v[24:25] op_sel_hi:[0,1,1]
	v_pk_fma_f32 v[8:9], v[16:17], v[14:15], v[8:9] op_sel_hi:[0,1,1]
	v_cvt_pk_f16_f32 v4, v6, v7
	v_cvt_pk_f16_f32 v5, v12, v13
	v_cvt_pk_f16_f32 v6, v18, v19
	v_cvt_pk_f16_f32 v7, v8, v9
	global_store_dwordx4 v[2:3], v[4:7], off sc1

.LBB1_273:
	v_add_f32_e32 v67, v50, v51
	v_add_f32_e32 v67, v52, v67
	ds_read_b64_tr_b16 v[68:69], v206 offset:40960
	ds_read_b64_tr_b16 v[70:71], v206 offset:41472
	v_add_f32_e32 v67, v53, v67
	v_add_f32_e32 v67, v54, v67
	v_add_f32_e32 v67, v55, v67
	v_add_f32_e32 v67, v56, v67
	v_add_f32_e32 v67, v57, v67
	v_cvt_pk_f16_f32 v50, v50, v51
	v_cvt_pk_f16_f32 v51, v52, v53
	v_cvt_pk_f16_f32 v52, v54, v55
	v_cvt_pk_f16_f32 v53, v56, v57
	ds_read_b64_tr_b16 v[54:55], v206 offset:41984
	ds_read_b64_tr_b16 v[56:57], v206 offset:42496
	s_waitcnt lgkmcnt(2)
	v_mfma_f32_32x32x16_f16 v[2:17], v[50:53], v[68:71], v[2:17]
	ds_read_b64_tr_b16 v[68:69], v206 offset:45056
	ds_read_b64_tr_b16 v[70:71], v206 offset:45568
	v_add_f32_e32 v67, v58, v67
	v_add_f32_e32 v67, v59, v67
	v_add_f32_e32 v67, v60, v67
	ds_read_b64_tr_b16 v[72:73], v206 offset:46080
	ds_read_b64_tr_b16 v[74:75], v206 offset:46592
	s_waitcnt lgkmcnt(2)
	v_mfma_f32_32x32x16_f16 v[18:33], v[50:53], v[68:71], v[18:33]
	v_add_f32_e32 v50, v61, v67
	v_add_f32_e32 v50, v62, v50
	v_add_f32_e32 v67, v63, v50
	v_cvt_pk_f16_f32 v50, v58, v59
	v_cvt_pk_f16_f32 v51, v60, v61
	v_cvt_pk_f16_f32 v52, v62, v63
	v_cvt_pk_f16_f32 v53, v64, v65
	s_nop 0
	v_mfma_f32_32x32x16_f16 v[2:17], v[50:53], v[54:57], v[2:17]
	v_add_f32_e32 v54, v64, v67
	v_add_f32_e32 v54, v65, v54
	v_add_f32_e32 v54, v34, v54
	v_add_f32_e32 v54, v35, v54
	v_add_f32_e32 v54, v36, v54
	v_add_f32_e32 v58, v37, v54
	v_cvt_pk_f16_f32 v34, v34, v35
	s_waitcnt lgkmcnt(0)
	v_mfma_f32_32x32x16_f16 v[18:33], v[50:53], v[72:75], v[18:33]
	ds_read_b64_tr_b16 v[50:51], v206 offset:43008
	ds_read_b64_tr_b16 v[52:53], v206 offset:43520
	v_cvt_pk_f16_f32 v35, v36, v37
	v_cvt_pk_f16_f32 v36, v38, v39
	v_cvt_pk_f16_f32 v37, v40, v41
	ds_read_b64_tr_b16 v[54:55], v206 offset:44032
	ds_read_b64_tr_b16 v[56:57], v206 offset:44544
	v_add_f32_e32 v38, v38, v58
	v_add_f32_e32 v38, v39, v38
	s_waitcnt lgkmcnt(2)
	v_mfma_f32_32x32x16_f16 v[2:17], v[34:37], v[50:53], v[2:17]
	ds_read_b64_tr_b16 v[50:51], v206 offset:47104
	ds_read_b64_tr_b16 v[52:53], v206 offset:47616
	v_add_f32_e32 v38, v40, v38
	ds_read_b64_tr_b16 v[58:59], v206 offset:48128
	ds_read_b64_tr_b16 v[60:61], v206 offset:48640
	v_cvt_pk_f16_f32 v39, v48, v49
	s_waitcnt lgkmcnt(2)
	v_mfma_f32_32x32x16_f16 v[18:33], v[34:37], v[50:53], v[18:33]
	v_add_f32_e32 v34, v41, v38
	v_add_f32_e32 v34, v42, v34
	v_add_f32_e32 v34, v43, v34
	v_add_f32_e32 v34, v44, v34
	v_cvt_pk_f16_f32 v36, v42, v43
	v_cvt_pk_f16_f32 v37, v44, v45
	v_cvt_pk_f16_f32 v38, v46, v47
	v_add_f32_e32 v34, v45, v34
	v_mfma_f32_32x32x16_f16 v[2:17], v[36:39], v[54:57], v[2:17]
	v_add_f32_e32 v34, v46, v34
	v_add_f32_e32 v34, v47, v34
	v_add_f32_e32 v34, v48, v34
	v_add_f32_e32 v34, v49, v34
	v_add_f32_e32 v34, v122, v34
	v_mov_b32_e32 v35, v34
	s_nop 1
	v_permlane32_swap_b32_e32 v34, v35
	s_waitcnt lgkmcnt(0)
	v_mfma_f32_32x32x16_f16 v[18:33], v[36:39], v[58:61], v[18:33]
	s_and_saveexec_b64 s[2:3], s[0:1]
	v_add_f32_e32 v34, v34, v35
	ds_write_b32 v207, v34 offset:49280
	s_or_b64 exec, exec, s[2:3]
	s_waitcnt lgkmcnt(0)
	ds_read_b128 v[34:37], v66 offset:49280
	ds_read_b128 v[38:41], v66 offset:49312
	s_lshl_b32 s0, s39, 1
	s_add_u32 s2, s14, s0
	s_addc_u32 s3, s15, 0
	s_waitcnt lgkmcnt(1)
	v_rcp_f32_e32 v42, v34
	v_rcp_f32_e32 v43, v35
	s_lshl_b32 s0, s38, 12
	s_add_i32 s8, s0, 0
	v_lshlrev_b32_e32 v50, 9, v210
	v_lshlrev_b32_e32 v51, 1, v211
	v_rcp_f32_e32 v44, v36
	v_add3_u32 v50, s8, v50, v51
	v_fma_mixlo_f16 v2, v2, v42, 0
	ds_write_b16 v50, v2
	v_fma_mixlo_f16 v2, v18, v42, 0
	v_rcp_f32_e32 v45, v37
	ds_write_b16 v50, v2 offset:64
	v_fma_mixlo_f16 v2, v3, v43, 0
	ds_write_b16 v50, v2 offset:128
	v_fma_mixlo_f16 v2, v19, v43, 0
	s_waitcnt lgkmcnt(3)
	v_rcp_f32_e32 v46, v38
	ds_write_b16 v50, v2 offset:192
	v_fma_mixlo_f16 v2, v4, v44, 0
	ds_write_b16 v50, v2 offset:256
	v_fma_mixlo_f16 v2, v20, v44, 0
	v_rcp_f32_e32 v47, v39
	ds_write_b16 v50, v2 offset:320
	v_fma_mixlo_f16 v2, v5, v45, 0
	ds_read_b128 v[34:37], v66 offset:49344
	ds_write_b16 v50, v2 offset:384
	v_fma_mixlo_f16 v2, v21, v45, 0
	v_rcp_f32_e32 v48, v40
	ds_write_b16 v50, v2 offset:448
	v_fma_mixlo_f16 v2, v6, v46, 0
	ds_write_b16 v50, v2 offset:1024
	v_fma_mixlo_f16 v2, v22, v46, 0
	v_rcp_f32_e32 v49, v41
	ds_write_b16 v50, v2 offset:1088
	v_fma_mixlo_f16 v2, v7, v47, 0
	ds_write_b16 v50, v2 offset:1152
	v_fma_mixlo_f16 v2, v23, v47, 0
	ds_read_b128 v[38:41], v66 offset:49376
	s_waitcnt lgkmcnt(6)
	v_rcp_f32_e32 v34, v34
	ds_write_b16 v50, v2 offset:1216
	v_fma_mixlo_f16 v2, v8, v48, 0
	ds_write_b16 v50, v2 offset:1280
	v_fma_mixlo_f16 v2, v24, v48, 0
	v_rcp_f32_e32 v35, v35
	ds_write_b16 v50, v2 offset:1344
	v_fma_mixlo_f16 v2, v9, v49, 0
	ds_write_b16 v50, v2 offset:1408
	v_fma_mixlo_f16 v2, v25, v49, 0
	v_rcp_f32_e32 v36, v36
	ds_write_b16 v50, v2 offset:1472
	v_fma_mixlo_f16 v2, v10, v34, 0
	ds_write_b16 v50, v2 offset:2048
	v_fma_mixlo_f16 v2, v26, v34, 0
	v_rcp_f32_e32 v37, v37
	ds_write_b16 v50, v2 offset:2112
	v_fma_mixlo_f16 v2, v11, v35, 0
	ds_write_b16 v50, v2 offset:2176
	v_fma_mixlo_f16 v2, v27, v35, 0
	s_waitcnt lgkmcnt(8)
	v_rcp_f32_e32 v38, v38
	ds_write_b16 v50, v2 offset:2240
	v_fma_mixlo_f16 v2, v12, v36, 0
	ds_write_b16 v50, v2 offset:2304
	v_fma_mixlo_f16 v2, v28, v36, 0
	v_rcp_f32_e32 v39, v39
	ds_write_b16 v50, v2 offset:2368
	v_fma_mixlo_f16 v2, v13, v37, 0
	ds_write_b16 v50, v2 offset:2432
	v_fma_mixlo_f16 v2, v29, v37, 0
	v_rcp_f32_e32 v40, v40
	ds_write_b16 v50, v2 offset:2496
	v_fma_mixlo_f16 v2, v14, v38, 0
	ds_write_b16 v50, v2 offset:3072
	v_fma_mixlo_f16 v2, v30, v38, 0
	v_rcp_f32_e32 v41, v41
	ds_write_b16 v50, v2 offset:3136
	v_fma_mixlo_f16 v2, v15, v39, 0
	ds_write_b16 v50, v2 offset:3200
	v_fma_mixlo_f16 v2, v31, v39, 0
	ds_write_b16 v50, v2 offset:3264
	v_fma_mixlo_f16 v2, v16, v40, 0
	ds_write_b16 v50, v2 offset:3328
	v_fma_mixlo_f16 v2, v32, v40, 0
	ds_write_b16 v50, v2 offset:3392
	v_fma_mixlo_f16 v2, v17, v41, 0
	ds_write_b16 v50, v2 offset:3456
	v_fma_mixlo_f16 v2, v33, v41, 0
	s_lshl_b64 s[0:1], s[6:7], 1
	ds_write_b16 v50, v2 offset:3520
	s_add_u32 s0, s2, s0
	v_lshlrev_b32_e32 v2, 4, v1
	v_lshlrev_b32_e32 v20, 7, v199
	s_addc_u32 s1, s3, s1
	s_waitcnt lgkmcnt(0)
	v_mov_b32_e32 v3, 0
	v_add3_u32 v14, s8, v2, v20
	v_lshl_add_u64 v[18:19], s[0:1], 0, v[2:3]
	v_mov_b32_e32 v21, v3
	ds_read_b128 v[2:5], v14
	ds_read_b128 v[6:9], v14 offset:1024
	ds_read_b128 v[10:13], v14 offset:2048
	ds_read_b128 v[14:17], v14 offset:3072
	v_lshl_add_u64 v[18:19], v[18:19], 0, v[20:21]
	s_waitcnt lgkmcnt(3)
	global_store_dwordx4 v[18:19], v[2:5], off sc1
	s_waitcnt lgkmcnt(2)
	global_store_dwordx4 v[18:19], v[6:9], off offset:1024 sc1
	s_waitcnt lgkmcnt(1)
	global_store_dwordx4 v[18:19], v[10:13], off offset:2048 sc1
	s_waitcnt lgkmcnt(0)
	global_store_dwordx4 v[18:19], v[14:17], off offset:3072 sc1
	s_waitcnt lgkmcnt(0)
	s_barrier
	v_mov_b32_e32 v200, v1
.LBB1_276:
	s_nop 0
	v_ashrrev_i32_e32 v6, 7, v198
	v_lshlrev_b32_e32 v0, 7, v0
	v_and_b32_e32 v0, 0x3c00, v0
	v_mov_b32_e32 v1, 0
	v_ashrrev_i32_e32 v7, 31, v6
	v_lshl_add_u64 v[6:7], v[6:7], 0, v[0:1]
	v_mov_b32_e32 v201, v1
	v_lshlrev_b64 v[0:1], 7, v[6:7]
	s_waitcnt lgkmcnt(0)
	v_lshl_add_u64 v[0:1], s[4:5], 0, v[0:1]
	s_waitcnt vmcnt(1)
	v_cvt_pk_f16_f32 v5, v136, v137
	v_cvt_pk_f16_f32 v4, v134, v135
	s_waitcnt vmcnt(0)
	v_cvt_pk_f16_f32 v3, v132, v133
	v_cvt_pk_f16_f32 v2, v130, v131
	v_lshl_add_u64 v[0:1], v[200:201], 4, v[0:1]
	global_store_dwordx4 v[0:1], v[2:5], off sc1
	s_endpgm

_Z11gemm_kernelILi256ELi192ELi4ELi2ELi4ELi2ELi2ELi0EEvPKDF16_S1_iiiPDF16_PfPK15HIP_vector_typeIfLj2EE:
	s_load_dwordx8 s[4:11], s[0:1], 0x0
	s_load_dwordx2 s[12:13], s[0:1], 0x30
	s_lshr_b32 s18, s2, 3
	v_readfirstlane_b32 s17, v0
	s_lshr_b32 s14, s17, 6
	s_waitcnt lgkmcnt(0)
	s_ashr_i32 s11, s8, 31
	s_lshr_b32 s3, s11, 22
	s_add_i32 s3, s8, s3
	s_ashr_i32 s15, s3, 10
	s_abs_i32 s16, s15
	v_cvt_f32_u32_e32 v1, s16
	s_sub_i32 s21, 0, s16
	s_mul_hi_i32 s19, s9, 0x2aaaaaab
	s_lshr_b32 s20, s19, 31
	v_rcp_iflag_f32_e32 v1, v1
	s_ashr_i32 s19, s19, 6
	s_add_i32 s19, s19, s20
	s_bfe_u32 s20, s2, 0x20001
	v_mul_f32_e32 v1, 0x4f7ffffe, v1
	v_cvt_u32_f32_e32 v1, v1
	s_ashr_i32 s3, s3, 31
	s_mul_i32 s20, s15, s20
	v_mov_b32_e32 v97, 0
	v_readfirstlane_b32 s22, v1
	s_mul_i32 s21, s21, s22
	s_mul_hi_u32 s21, s22, s21
	s_add_i32 s22, s22, s21
	s_mul_hi_u32 s22, s18, s22
	s_mul_i32 s21, s22, s16
	s_sub_i32 s23, s18, s21
	s_add_i32 s24, s22, 1
	s_sub_i32 s25, s23, s16
	s_cmp_ge_u32 s23, s16
	s_cselect_b32 s22, s24, s22
	s_cselect_b32 s23, s25, s23
	s_add_i32 s24, s22, 1
	s_cmp_ge_u32 s23, s16
	s_cselect_b32 s16, s24, s22
	s_xor_b32 s16, s16, s3
	s_sub_i32 s3, s16, s3
	s_mul_i32 s15, s3, s15
	s_sub_i32 s15, s18, s15
	s_add_i32 s15, s15, s20
	s_bitcmp1_b32 s2, 0
	v_bfe_u32 v1, v0, 3, 3
	s_cselect_b32 s2, s19, 0
	v_lshl_or_b32 v1, s14, 3, v1
	s_add_i32 s18, s3, s2
	s_lshl_b32 s19, s15, 8
	v_lshrrev_b32_e32 v2, 1, v1
	s_lshl_b32 s2, s14, 10
	v_xor_b32_e32 v6, v2, v0
	v_add_u32_e32 v2, s19, v1
	s_cmp_lg_u32 0, -1
	s_mul_i32 s15, s18, 0xc0
	v_ashrrev_i32_e32 v3, 31, v2
	s_cselect_b32 s3, 0, 0
	v_lshlrev_b64 v[2:3], 7, v[2:3]
	v_add_u32_e32 v4, s15, v1
	s_add_i32 s22, s2, s3
	v_lshlrev_b32_e32 v1, 4, v6
	s_lshr_b32 s3, s17, 1
	v_lshl_add_u64 v[2:3], s[4:5], 0, v[2:3]
	v_ashrrev_i32_e32 v5, 31, v4
	v_and_b32_e32 v96, 0x70, v1
	s_add_i32 s24, s22, 0x8000
	s_and_b32 s20, s3, 0x7fffffc0
	v_lshlrev_b64 v[4:5], 7, v[4:5]
	v_lshl_add_u64 v[104:105], v[2:3], 0, v[96:97]
	s_bitcmp1_b32 s17, 6
	s_mov_b64 s[4:5], 0x2000
	s_mov_b32 m0, s22
	s_nop 0
	global_load_lds_dwordx4 v[104:105], off
	v_lshl_add_u64 v[4:5], s[6:7], 0, v[4:5]
	s_cselect_b32 s16, 0x60, 0
	v_lshl_add_u64 v[110:111], v[104:105], 0, s[4:5]
	s_mov_b64 s[6:7], 0x4000
	s_add_i32 s3, s22, 0x2000
	s_mov_b32 m0, s3
	s_nop 0
	global_load_lds_dwordx4 v[110:111], off
	v_lshl_add_u64 v[108:109], v[104:105], 0, s[6:7]
	s_mov_b64 s[26:27], 0x6000
	s_add_i32 s3, s22, 0x4000
	s_mov_b32 m0, s3
	s_nop 0
	global_load_lds_dwordx4 v[108:109], off
	v_lshl_add_u64 v[106:107], v[104:105], 0, s[26:27]
	s_add_i32 s3, s22, 0x6000
	s_mov_b32 m0, s3
	s_nop 0
	global_load_lds_dwordx4 v[106:107], off
	v_lshl_add_u64 v[98:99], v[4:5], 0, v[96:97]
	s_mov_b32 m0, s24
	s_nop 0
	global_load_lds_dwordx4 v[98:99], off
	v_lshl_add_u64 v[100:101], v[98:99], 0, s[4:5]
	s_add_i32 s3, s22, 0xa000
	s_mov_b32 m0, s3
	s_nop 0
	global_load_lds_dwordx4 v[100:101], off
	v_lshl_add_u64 v[102:103], v[98:99], 0, s[6:7]
	s_add_i32 s3, s22, 0xc000
	s_mov_b32 m0, s3
	s_nop 0
	global_load_lds_dwordx4 v[102:103], off
	s_mov_b32 s21, 1
	s_mov_b32 s23, 0
	s_cmp_lt_i32 s10, 64
	v_mov_b32_e32 v96, v97
	v_mov_b32_e32 v95, v97
	v_mov_b32_e32 v94, v97
	v_mov_b32_e32 v93, v97
	v_mov_b32_e32 v92, v97
	v_mov_b32_e32 v91, v97
	v_mov_b32_e32 v90, v97
	v_mov_b32_e32 v89, v97
	v_mov_b32_e32 v88, v97
	v_mov_b32_e32 v87, v97
	v_mov_b32_e32 v86, v97
	v_mov_b32_e32 v85, v97
	v_mov_b32_e32 v84, v97
	v_mov_b32_e32 v83, v97
	v_mov_b32_e32 v82, v97
	v_mov_b32_e32 v81, v97
	v_mov_b32_e32 v80, v97
	v_mov_b32_e32 v79, v97
	v_mov_b32_e32 v78, v97
	v_mov_b32_e32 v77, v97
	v_mov_b32_e32 v76, v97
	v_mov_b32_e32 v75, v97
	v_mov_b32_e32 v74, v97
	v_mov_b32_e32 v73, v97
	v_mov_b32_e32 v72, v97
	v_mov_b32_e32 v71, v97
	v_mov_b32_e32 v70, v97
	v_mov_b32_e32 v69, v97
	v_mov_b32_e32 v68, v97
	v_mov_b32_e32 v67, v97
	v_mov_b32_e32 v66, v97
	v_mov_b32_e32 v65, v97
	v_mov_b32_e32 v64, v97
	v_mov_b32_e32 v63, v97
	v_mov_b32_e32 v62, v97
	v_mov_b32_e32 v61, v97
	v_mov_b32_e32 v60, v97
	v_mov_b32_e32 v59, v97
	v_mov_b32_e32 v58, v97
	v_mov_b32_e32 v57, v97
	v_mov_b32_e32 v56, v97
	v_mov_b32_e32 v55, v97
	v_mov_b32_e32 v54, v97
	v_mov_b32_e32 v53, v97
	v_mov_b32_e32 v52, v97
	v_mov_b32_e32 v51, v97
	v_mov_b32_e32 v50, v97
	v_mov_b32_e32 v49, v97
	v_mov_b32_e32 v48, v97
	v_mov_b32_e32 v47, v97
	v_mov_b32_e32 v46, v97
	v_mov_b32_e32 v45, v97
	v_mov_b32_e32 v44, v97
	v_mov_b32_e32 v43, v97
	v_mov_b32_e32 v42, v97
	v_mov_b32_e32 v41, v97
	v_mov_b32_e32 v40, v97
	v_mov_b32_e32 v39, v97
	v_mov_b32_e32 v38, v97
	v_mov_b32_e32 v37, v97
	v_mov_b32_e32 v36, v97
	v_mov_b32_e32 v35, v97
	v_mov_b32_e32 v34, v97
	v_mov_b32_e32 v33, v97
	v_mov_b32_e32 v32, v97
	v_mov_b32_e32 v31, v97
	v_mov_b32_e32 v30, v97
	v_mov_b32_e32 v29, v97
	v_mov_b32_e32 v28, v97
	v_mov_b32_e32 v27, v97
	v_mov_b32_e32 v26, v97
	v_mov_b32_e32 v25, v97
	v_mov_b32_e32 v24, v97
	v_mov_b32_e32 v23, v97
	v_mov_b32_e32 v22, v97
	v_mov_b32_e32 v21, v97
	v_mov_b32_e32 v20, v97
	v_mov_b32_e32 v19, v97
	v_mov_b32_e32 v18, v97
	v_mov_b32_e32 v17, v97
	v_mov_b32_e32 v16, v97
	v_mov_b32_e32 v15, v97
	v_mov_b32_e32 v14, v97
	v_mov_b32_e32 v13, v97
	v_mov_b32_e32 v12, v97
	v_mov_b32_e32 v11, v97
	v_mov_b32_e32 v10, v97
	v_mov_b32_e32 v9, v97
	v_mov_b32_e32 v8, v97
	v_mov_b32_e32 v7, v97
	v_mov_b32_e32 v6, v97
	v_mov_b32_e32 v5, v97
	v_mov_b32_e32 v4, v97
	v_mov_b32_e32 v3, v97
	v_mov_b32_e32 v2, v97
	v_and_b32_e32 v162, 31, v0
	v_bfe_u32 v1, v0, 5, 1
	s_cbranch_scc1 .LBB2_6
	s_ashr_i32 s3, s10, 31
	s_lshr_b32 s3, s3, 26
	s_add_i32 s3, s10, s3
	v_lshrrev_b32_e32 v2, 1, v0
	s_ashr_i32 s25, s3, 6
	v_bitop3_b32 v2, v1, v2, 7 bitop3:0x78
	s_cmp_lg_u32 0, -1
	v_lshlrev_b32_e32 v120, 4, v2
	v_or_b32_e32 v2, s20, v162
	s_cselect_b32 s3, 0, 0
	v_lshl_add_u32 v121, v2, 7, 0
	v_or_b32_e32 v2, s16, v162
	s_mov_b32 s10, s8
	s_add_i32 s8, s3, s2
	s_ashr_i32 s3, s9, 31
	s_mov_b32 s2, s9
	v_lshl_add_u32 v122, v2, 7, 0
	s_lshl_b64 s[2:3], s[2:3], 7
	v_mov_b32_e32 v2, 0
	s_addk_i32 s8, 0x6000
	v_xor_b32_e32 v123, 32, v120
	v_xor_b32_e32 v124, 64, v120
	v_xor_b32_e32 v125, 0x60, v120
	s_lshl_b64 s[4:5], s[10:11], 7
	s_mov_b64 s[6:7], s[2:3]
	s_mov_b32 s9, 0
	v_mov_b32_e32 v3, v2
	v_mov_b32_e32 v4, v2
	v_mov_b32_e32 v5, v2
	v_mov_b32_e32 v6, v2
	v_mov_b32_e32 v7, v2
	v_mov_b32_e32 v8, v2
	v_mov_b32_e32 v9, v2
	v_mov_b32_e32 v10, v2
	v_mov_b32_e32 v11, v2
	v_mov_b32_e32 v12, v2
	v_mov_b32_e32 v13, v2
	v_mov_b32_e32 v14, v2
	v_mov_b32_e32 v15, v2
	v_mov_b32_e32 v16, v2
	v_mov_b32_e32 v17, v2
	v_mov_b32_e32 v18, v2
	v_mov_b32_e32 v19, v2
	v_mov_b32_e32 v20, v2
	v_mov_b32_e32 v21, v2
	v_mov_b32_e32 v22, v2
	v_mov_b32_e32 v23, v2
	v_mov_b32_e32 v24, v2
	v_mov_b32_e32 v25, v2
	v_mov_b32_e32 v26, v2
	v_mov_b32_e32 v27, v2
	v_mov_b32_e32 v28, v2
	v_mov_b32_e32 v29, v2
	v_mov_b32_e32 v30, v2
	v_mov_b32_e32 v31, v2
	v_mov_b32_e32 v32, v2
	v_mov_b32_e32 v33, v2
	v_mov_b32_e32 v34, v2
	v_mov_b32_e32 v35, v2
	v_mov_b32_e32 v36, v2
	v_mov_b32_e32 v37, v2
	v_mov_b32_e32 v38, v2
	v_mov_b32_e32 v39, v2
	v_mov_b32_e32 v40, v2
	v_mov_b32_e32 v41, v2
	v_mov_b32_e32 v42, v2
	v_mov_b32_e32 v43, v2
	v_mov_b32_e32 v44, v2
	v_mov_b32_e32 v45, v2
	v_mov_b32_e32 v46, v2
	v_mov_b32_e32 v47, v2
	v_mov_b32_e32 v48, v2
	v_mov_b32_e32 v49, v2
	v_mov_b32_e32 v50, v2
	v_mov_b32_e32 v51, v2
	v_mov_b32_e32 v52, v2
	v_mov_b32_e32 v53, v2
	v_mov_b32_e32 v54, v2
	v_mov_b32_e32 v55, v2
	v_mov_b32_e32 v56, v2
	v_mov_b32_e32 v57, v2
	v_mov_b32_e32 v58, v2
	v_mov_b32_e32 v59, v2
	v_mov_b32_e32 v60, v2
	v_mov_b32_e32 v61, v2
	v_mov_b32_e32 v62, v2
	v_mov_b32_e32 v63, v2
	v_mov_b32_e32 v64, v2
	v_mov_b32_e32 v65, v2
	v_mov_b32_e32 v66, v2
	v_mov_b32_e32 v67, v2
	v_mov_b32_e32 v68, v2
	v_mov_b32_e32 v69, v2
	v_mov_b32_e32 v70, v2
	v_mov_b32_e32 v71, v2
	v_mov_b32_e32 v72, v2
	v_mov_b32_e32 v73, v2
	v_mov_b32_e32 v74, v2
	v_mov_b32_e32 v75, v2
	v_mov_b32_e32 v76, v2
	v_mov_b32_e32 v77, v2
	v_mov_b32_e32 v78, v2
	v_mov_b32_e32 v79, v2
	v_mov_b32_e32 v80, v2
	v_mov_b32_e32 v81, v2
	v_mov_b32_e32 v82, v2
	v_mov_b32_e32 v83, v2
	v_mov_b32_e32 v84, v2
	v_mov_b32_e32 v85, v2
	v_mov_b32_e32 v86, v2
	v_mov_b32_e32 v87, v2
	v_mov_b32_e32 v88, v2
	v_mov_b32_e32 v89, v2
	v_mov_b32_e32 v90, v2
	v_mov_b32_e32 v91, v2
	v_mov_b32_e32 v92, v2
	v_mov_b32_e32 v93, v2
	v_mov_b32_e32 v94, v2
	v_mov_b32_e32 v95, v2
	v_mov_b32_e32 v96, v2
	v_mov_b32_e32 v97, v2
	v_lshl_add_u64 v[168:169], v[104:105], 0, s[4:5]
	v_lshl_add_u64 v[170:171], v[110:111], 0, s[4:5]
	v_lshl_add_u64 v[172:173], v[108:109], 0, s[4:5]
	v_lshl_add_u64 v[174:175], v[106:107], 0, s[4:5]
	v_lshl_add_u64 v[176:177], v[98:99], 0, s[2:3]
	v_lshl_add_u64 v[178:179], v[100:101], 0, s[2:3]
	v_lshl_add_u64 v[180:181], v[102:103], 0, s[2:3]
	s_mov_b32 s9, 1
	s_add_i32 s25, s25, -1
	s_cmp_lt_u32 s14, 4
	s_cbranch_scc1 .Lqkv_a0
	s_waitcnt vmcnt(0) lgkmcnt(0)
	s_barrier
	s_mul_i32 s10, s23, 0xe000
	s_mul_i32 s11, s21, 0xe000
	v_add_u32_e32 v142, s10, v122
	v_add_u32_e32 v143, s10, v121
	s_add_i32 s11, s11, s22
	s_xor_b32 s23, s23, 1
	s_xor_b32 s21, s21, 1
	v_add_u32_e32 v144, v142, v120
	v_add_u32_e32 v145, v143, v120
	ds_read_b128 v[130:133], v145
	ds_read_b128 v[104:107], v144 offset:32768
	ds_read_b128 v[108:111], v144 offset:36864
	ds_read_b128 v[134:137], v145 offset:4096
	ds_read_b128 v[126:129], v144 offset:40960
	s_mov_b32 m0, s11
	s_nop 0
	global_load_lds_dwordx4 v[168:169], off
	v_lshl_add_u64 v[168:169], v[168:169], 0, s[4:5]
	s_add_i32 m0, s11, 0x2000
	s_nop 0
	global_load_lds_dwordx4 v[170:171], off
	v_lshl_add_u64 v[170:171], v[170:171], 0, s[4:5]
	s_add_i32 m0, s11, 0x4000
	s_nop 0
	global_load_lds_dwordx4 v[172:173], off
	v_lshl_add_u64 v[172:173], v[172:173], 0, s[4:5]
	v_add_u32_e32 v146, v142, v123
	v_add_u32_e32 v147, v143, v123
	ds_read_b128 v[182:185], v147
	ds_read_b128 v[138:141], v146 offset:32768
	ds_read_b128 v[112:115], v146 offset:36864
	ds_read_b128 v[186:189], v147 offset:4096
	ds_read_b128 v[116:119], v146 offset:40960
	s_waitcnt lgkmcnt(8)
	s_add_i32 m0, s11, 0x6000
	v_mfma_f32_32x32x16_f16 v[82:97], v[104:107], v[130:133], v[82:97]
	global_load_lds_dwordx4 v[174:175], off
	v_lshl_add_u64 v[174:175], v[174:175], 0, s[4:5]
	s_waitcnt lgkmcnt(7)
	v_mfma_f32_32x32x16_f16 v[66:81], v[108:111], v[130:133], v[66:81]
	s_waitcnt lgkmcnt(6)
	s_add_i32 m0, s11, 0x8000
	v_mfma_f32_32x32x16_f16 v[34:49], v[104:107], v[134:137], v[34:49]
	global_load_lds_dwordx4 v[176:177], off
	v_lshl_add_u64 v[176:177], v[176:177], 0, s[2:3]
	v_mfma_f32_32x32x16_f16 v[18:33], v[108:111], v[134:137], v[18:33]
	s_waitcnt lgkmcnt(5)
	s_add_i32 m0, s11, 0xa000
	v_mfma_f32_32x32x16_f16 v[50:65], v[126:129], v[130:133], v[50:65]
	global_load_lds_dwordx4 v[178:179], off
	v_lshl_add_u64 v[178:179], v[178:179], 0, s[2:3]
	v_mfma_f32_32x32x16_f16 v[2:17], v[126:129], v[134:137], v[2:17]
	v_add_u32_e32 v144, v142, v124
	v_add_u32_e32 v145, v143, v124
	ds_read_b128 v[130:133], v145
	ds_read_b128 v[104:107], v144 offset:32768
	ds_read_b128 v[108:111], v144 offset:36864
	ds_read_b128 v[134:137], v145 offset:4096
	ds_read_b128 v[126:129], v144 offset:40960
	s_waitcnt lgkmcnt(8)
	s_add_i32 m0, s11, 0xc000
	v_mfma_f32_32x32x16_f16 v[82:97], v[138:141], v[182:185], v[82:97]
	global_load_lds_dwordx4 v[180:181], off
	v_lshl_add_u64 v[180:181], v[180:181], 0, s[2:3]
	s_waitcnt lgkmcnt(7)
	v_mfma_f32_32x32x16_f16 v[66:81], v[112:115], v[182:185], v[66:81]
	s_waitcnt lgkmcnt(6)
	v_mfma_f32_32x32x16_f16 v[34:49], v[138:141], v[186:189], v[34:49]
	v_mfma_f32_32x32x16_f16 v[18:33], v[112:115], v[186:189], v[18:33]
	s_waitcnt lgkmcnt(5)
	v_mfma_f32_32x32x16_f16 v[50:65], v[116:119], v[182:185], v[50:65]
	v_mfma_f32_32x32x16_f16 v[2:17], v[116:119], v[186:189], v[2:17]
	v_add_u32_e32 v146, v142, v125
	v_add_u32_e32 v147, v143, v125
	ds_read_b128 v[182:185], v147
	ds_read_b128 v[138:141], v146 offset:32768
	ds_read_b128 v[112:115], v146 offset:36864
	ds_read_b128 v[186:189], v147 offset:4096
	ds_read_b128 v[116:119], v146 offset:40960
	s_waitcnt lgkmcnt(8)
	v_mfma_f32_32x32x16_f16 v[82:97], v[104:107], v[130:133], v[82:97]
	s_waitcnt lgkmcnt(7)
	v_mfma_f32_32x32x16_f16 v[66:81], v[108:111], v[130:133], v[66:81]
	s_waitcnt lgkmcnt(6)
	v_mfma_f32_32x32x16_f16 v[34:49], v[104:107], v[134:137], v[34:49]
	v_mfma_f32_32x32x16_f16 v[18:33], v[108:111], v[134:137], v[18:33]
	s_waitcnt lgkmcnt(5)
	v_mfma_f32_32x32x16_f16 v[50:65], v[126:129], v[130:133], v[50:65]
	v_mfma_f32_32x32x16_f16 v[2:17], v[126:129], v[134:137], v[2:17]
.Lqkv_loop:
	s_waitcnt vmcnt(0) lgkmcnt(0)
	s_barrier
	s_mul_i32 s10, s23, 0xe000
	s_mul_i32 s11, s21, 0xe000
	v_add_u32_e32 v142, s10, v122
	v_add_u32_e32 v143, s10, v121
	s_add_i32 s11, s11, s22
	s_xor_b32 s23, s23, 1
	s_xor_b32 s21, s21, 1
	v_add_u32_e32 v144, v142, v120
	v_add_u32_e32 v145, v143, v120
	ds_read_b128 v[130:133], v145
	ds_read_b128 v[104:107], v144 offset:32768
	ds_read_b128 v[108:111], v144 offset:36864
	ds_read_b128 v[134:137], v145 offset:4096
	ds_read_b128 v[126:129], v144 offset:40960
	s_mov_b32 m0, s11
	v_mfma_f32_32x32x16_f16 v[82:97], v[138:141], v[182:185], v[82:97]
	global_load_lds_dwordx4 v[168:169], off
	v_lshl_add_u64 v[168:169], v[168:169], 0, s[4:5]
	v_mfma_f32_32x32x16_f16 v[66:81], v[112:115], v[182:185], v[66:81]
	s_add_i32 m0, s11, 0x2000
	v_mfma_f32_32x32x16_f16 v[34:49], v[138:141], v[186:189], v[34:49]
	global_load_lds_dwordx4 v[170:171], off
	v_lshl_add_u64 v[170:171], v[170:171], 0, s[4:5]
	v_mfma_f32_32x32x16_f16 v[18:33], v[112:115], v[186:189], v[18:33]
	s_add_i32 m0, s11, 0x4000
	v_mfma_f32_32x32x16_f16 v[50:65], v[116:119], v[182:185], v[50:65]
	global_load_lds_dwordx4 v[172:173], off
	v_lshl_add_u64 v[172:173], v[172:173], 0, s[4:5]
	v_mfma_f32_32x32x16_f16 v[2:17], v[116:119], v[186:189], v[2:17]
	v_add_u32_e32 v146, v142, v123
	v_add_u32_e32 v147, v143, v123
	ds_read_b128 v[182:185], v147
	ds_read_b128 v[138:141], v146 offset:32768
	ds_read_b128 v[112:115], v146 offset:36864
	ds_read_b128 v[186:189], v147 offset:4096
	ds_read_b128 v[116:119], v146 offset:40960
	s_waitcnt lgkmcnt(8)
	s_add_i32 m0, s11, 0x6000
	v_mfma_f32_32x32x16_f16 v[82:97], v[104:107], v[130:133], v[82:97]
	global_load_lds_dwordx4 v[174:175], off
	v_lshl_add_u64 v[174:175], v[174:175], 0, s[4:5]
	s_waitcnt lgkmcnt(7)
	v_mfma_f32_32x32x16_f16 v[66:81], v[108:111], v[130:133], v[66:81]
	s_waitcnt lgkmcnt(6)
	s_add_i32 m0, s11, 0x8000
	v_mfma_f32_32x32x16_f16 v[34:49], v[104:107], v[134:137], v[34:49]
	global_load_lds_dwordx4 v[176:177], off
	v_lshl_add_u64 v[176:177], v[176:177], 0, s[2:3]
	v_mfma_f32_32x32x16_f16 v[18:33], v[108:111], v[134:137], v[18:33]
	s_waitcnt lgkmcnt(5)
	s_add_i32 m0, s11, 0xa000
	v_mfma_f32_32x32x16_f16 v[50:65], v[126:129], v[130:133], v[50:65]
	global_load_lds_dwordx4 v[178:179], off
	v_lshl_add_u64 v[178:179], v[178:179], 0, s[2:3]
	v_mfma_f32_32x32x16_f16 v[2:17], v[126:129], v[134:137], v[2:17]
	v_add_u32_e32 v144, v142, v124
	v_add_u32_e32 v145, v143, v124
	ds_read_b128 v[130:133], v145
	ds_read_b128 v[104:107], v144 offset:32768
	ds_read_b128 v[108:111], v144 offset:36864
	ds_read_b128 v[134:137], v145 offset:4096
	ds_read_b128 v[126:129], v144 offset:40960
	s_waitcnt lgkmcnt(8)
	s_add_i32 m0, s11, 0xc000
	v_mfma_f32_32x32x16_f16 v[82:97], v[138:141], v[182:185], v[82:97]
	global_load_lds_dwordx4 v[180:181], off
	v_lshl_add_u64 v[180:181], v[180:181], 0, s[2:3]
	s_waitcnt lgkmcnt(7)
	v_mfma_f32_32x32x16_f16 v[66:81], v[112:115], v[182:185], v[66:81]
	s_waitcnt lgkmcnt(6)
	v_mfma_f32_32x32x16_f16 v[34:49], v[138:141], v[186:189], v[34:49]
	v_mfma_f32_32x32x16_f16 v[18:33], v[112:115], v[186:189], v[18:33]
	s_waitcnt lgkmcnt(5)
	v_mfma_f32_32x32x16_f16 v[50:65], v[116:119], v[182:185], v[50:65]
	v_mfma_f32_32x32x16_f16 v[2:17], v[116:119], v[186:189], v[2:17]
	v_add_u32_e32 v146, v142, v125
	v_add_u32_e32 v147, v143, v125
	ds_read_b128 v[182:185], v147
	ds_read_b128 v[138:141], v146 offset:32768
	ds_read_b128 v[112:115], v146 offset:36864
	ds_read_b128 v[186:189], v147 offset:4096
	ds_read_b128 v[116:119], v146 offset:40960
	s_waitcnt lgkmcnt(8)
	v_mfma_f32_32x32x16_f16 v[82:97], v[104:107], v[130:133], v[82:97]
	s_waitcnt lgkmcnt(7)
	v_mfma_f32_32x32x16_f16 v[66:81], v[108:111], v[130:133], v[66:81]
	s_waitcnt lgkmcnt(6)
	v_mfma_f32_32x32x16_f16 v[34:49], v[104:107], v[134:137], v[34:49]
	v_mfma_f32_32x32x16_f16 v[18:33], v[108:111], v[134:137], v[18:33]
	s_waitcnt lgkmcnt(5)
	v_mfma_f32_32x32x16_f16 v[50:65], v[126:129], v[130:133], v[50:65]
	v_mfma_f32_32x32x16_f16 v[2:17], v[126:129], v[134:137], v[2:17]
	s_add_i32 s9, s9, 1
	s_cmp_lt_i32 s9, s25
	s_cbranch_scc1 .Lqkv_loop
	s_waitcnt vmcnt(0) lgkmcnt(0)
	s_barrier
	s_mul_i32 s10, s23, 0xe000
	v_add_u32_e32 v142, s10, v122
	v_add_u32_e32 v143, s10, v121
	s_xor_b32 s23, s23, 1
	s_xor_b32 s21, s21, 1
	v_add_u32_e32 v144, v142, v120
	v_add_u32_e32 v145, v143, v120
	ds_read_b128 v[130:133], v145
	ds_read_b128 v[104:107], v144 offset:32768
	ds_read_b128 v[108:111], v144 offset:36864
	ds_read_b128 v[134:137], v145 offset:4096
	ds_read_b128 v[126:129], v144 offset:40960
	v_mfma_f32_32x32x16_f16 v[82:97], v[138:141], v[182:185], v[82:97]
	v_mfma_f32_32x32x16_f16 v[66:81], v[112:115], v[182:185], v[66:81]
	v_mfma_f32_32x32x16_f16 v[34:49], v[138:141], v[186:189], v[34:49]
	v_mfma_f32_32x32x16_f16 v[18:33], v[112:115], v[186:189], v[18:33]
	v_mfma_f32_32x32x16_f16 v[50:65], v[116:119], v[182:185], v[50:65]
	v_mfma_f32_32x32x16_f16 v[2:17], v[116:119], v[186:189], v[2:17]
	v_add_u32_e32 v146, v142, v123
	v_add_u32_e32 v147, v143, v123
	ds_read_b128 v[182:185], v147
	ds_read_b128 v[138:141], v146 offset:32768
	ds_read_b128 v[112:115], v146 offset:36864
	ds_read_b128 v[186:189], v147 offset:4096
	ds_read_b128 v[116:119], v146 offset:40960
	s_waitcnt lgkmcnt(8)
	v_mfma_f32_32x32x16_f16 v[82:97], v[104:107], v[130:133], v[82:97]
	s_waitcnt lgkmcnt(7)
	v_mfma_f32_32x32x16_f16 v[66:81], v[108:111], v[130:133], v[66:81]
	s_waitcnt lgkmcnt(6)
	v_mfma_f32_32x32x16_f16 v[34:49], v[104:107], v[134:137], v[34:49]
	v_mfma_f32_32x32x16_f16 v[18:33], v[108:111], v[134:137], v[18:33]
	s_waitcnt lgkmcnt(5)
	v_mfma_f32_32x32x16_f16 v[50:65], v[126:129], v[130:133], v[50:65]
	v_mfma_f32_32x32x16_f16 v[2:17], v[126:129], v[134:137], v[2:17]
	v_add_u32_e32 v144, v142, v124
	v_add_u32_e32 v145, v143, v124
	ds_read_b128 v[130:133], v145
	ds_read_b128 v[104:107], v144 offset:32768
	ds_read_b128 v[108:111], v144 offset:36864
	ds_read_b128 v[134:137], v145 offset:4096
	ds_read_b128 v[126:129], v144 offset:40960
	s_waitcnt lgkmcnt(8)
	v_mfma_f32_32x32x16_f16 v[82:97], v[138:141], v[182:185], v[82:97]
	s_waitcnt lgkmcnt(7)
	v_mfma_f32_32x32x16_f16 v[66:81], v[112:115], v[182:185], v[66:81]
	s_waitcnt lgkmcnt(6)
	v_mfma_f32_32x32x16_f16 v[34:49], v[138:141], v[186:189], v[34:49]
	v_mfma_f32_32x32x16_f16 v[18:33], v[112:115], v[186:189], v[18:33]
	s_waitcnt lgkmcnt(5)
	v_mfma_f32_32x32x16_f16 v[50:65], v[116:119], v[182:185], v[50:65]
	v_mfma_f32_32x32x16_f16 v[2:17], v[116:119], v[186:189], v[2:17]
	v_add_u32_e32 v146, v142, v125
	v_add_u32_e32 v147, v143, v125
	ds_read_b128 v[182:185], v147
	ds_read_b128 v[138:141], v146 offset:32768
	ds_read_b128 v[112:115], v146 offset:36864
	ds_read_b128 v[186:189], v147 offset:4096
	ds_read_b128 v[116:119], v146 offset:40960
	s_waitcnt lgkmcnt(8)
	v_mfma_f32_32x32x16_f16 v[82:97], v[104:107], v[130:133], v[82:97]
	s_waitcnt lgkmcnt(7)
	v_mfma_f32_32x32x16_f16 v[66:81], v[108:111], v[130:133], v[66:81]
	s_waitcnt lgkmcnt(6)
	v_mfma_f32_32x32x16_f16 v[34:49], v[104:107], v[134:137], v[34:49]
	v_mfma_f32_32x32x16_f16 v[18:33], v[108:111], v[134:137], v[18:33]
	s_waitcnt lgkmcnt(5)
	v_mfma_f32_32x32x16_f16 v[50:65], v[126:129], v[130:133], v[50:65]
	v_mfma_f32_32x32x16_f16 v[2:17], v[126:129], v[134:137], v[2:17]
	s_waitcnt lgkmcnt(0)
	v_mfma_f32_32x32x16_f16 v[82:97], v[138:141], v[182:185], v[82:97]
	v_mfma_f32_32x32x16_f16 v[66:81], v[112:115], v[182:185], v[66:81]
	v_mfma_f32_32x32x16_f16 v[34:49], v[138:141], v[186:189], v[34:49]
	v_mfma_f32_32x32x16_f16 v[18:33], v[112:115], v[186:189], v[18:33]
	v_mfma_f32_32x32x16_f16 v[50:65], v[116:119], v[182:185], v[50:65]
	v_mfma_f32_32x32x16_f16 v[2:17], v[116:119], v[186:189], v[2:17]
	s_branch .LBB2_6
.Lqkv_a0:
	s_mov_b32 s9, 0
.Lqkv_aloop:
	s_waitcnt vmcnt(0)
	s_barrier
	s_mul_i32 s10, s23, 0xe000
	s_mul_i32 s11, s21, 0xe000
	v_add_u32_e32 v142, s10, v122
	v_add_u32_e32 v143, s10, v121
	s_add_i32 s11, s11, s22
	s_xor_b32 s23, s23, 1
	s_xor_b32 s21, s21, 1
	v_add_u32_e32 v144, v142, v120
	v_add_u32_e32 v145, v143, v120
	ds_read_b128 v[130:133], v145
	ds_read_b128 v[104:107], v144 offset:32768
	ds_read_b128 v[108:111], v144 offset:36864
	ds_read_b128 v[134:137], v145 offset:4096
	ds_read_b128 v[126:129], v144 offset:40960
	s_mov_b32 m0, s11
	s_nop 0
	global_load_lds_dwordx4 v[168:169], off
	v_lshl_add_u64 v[168:169], v[168:169], 0, s[4:5]
	s_add_i32 m0, s11, 0x2000
	s_nop 0
	global_load_lds_dwordx4 v[170:171], off
	v_lshl_add_u64 v[170:171], v[170:171], 0, s[4:5]
	v_add_u32_e32 v146, v142, v123
	v_add_u32_e32 v147, v143, v123
	ds_read_b128 v[182:185], v147
	ds_read_b128 v[138:141], v146 offset:32768
	ds_read_b128 v[112:115], v146 offset:36864
	ds_read_b128 v[186:189], v147 offset:4096
	ds_read_b128 v[116:119], v146 offset:40960
	s_waitcnt lgkmcnt(8)
	s_add_i32 m0, s11, 0x4000
	v_mfma_f32_32x32x16_f16 v[82:97], v[104:107], v[130:133], v[82:97]
	global_load_lds_dwordx4 v[172:173], off
	v_lshl_add_u64 v[172:173], v[172:173], 0, s[4:5]
	s_waitcnt lgkmcnt(7)
	v_mfma_f32_32x32x16_f16 v[66:81], v[108:111], v[130:133], v[66:81]
	s_waitcnt lgkmcnt(6)
	s_add_i32 m0, s11, 0x6000
	v_mfma_f32_32x32x16_f16 v[34:49], v[104:107], v[134:137], v[34:49]
	global_load_lds_dwordx4 v[174:175], off
	v_lshl_add_u64 v[174:175], v[174:175], 0, s[4:5]
	v_mfma_f32_32x32x16_f16 v[18:33], v[108:111], v[134:137], v[18:33]
	s_waitcnt lgkmcnt(5)
	v_mfma_f32_32x32x16_f16 v[50:65], v[126:129], v[130:133], v[50:65]
	v_mfma_f32_32x32x16_f16 v[2:17], v[126:129], v[134:137], v[2:17]
	v_add_u32_e32 v144, v142, v124
	v_add_u32_e32 v145, v143, v124
	ds_read_b128 v[130:133], v145
	ds_read_b128 v[104:107], v144 offset:32768
	ds_read_b128 v[108:111], v144 offset:36864
	ds_read_b128 v[134:137], v145 offset:4096
	ds_read_b128 v[126:129], v144 offset:40960
	s_waitcnt lgkmcnt(8)
	s_add_i32 m0, s11, 0x8000
	v_mfma_f32_32x32x16_f16 v[82:97], v[138:141], v[182:185], v[82:97]
	global_load_lds_dwordx4 v[176:177], off
	v_lshl_add_u64 v[176:177], v[176:177], 0, s[2:3]
	s_waitcnt lgkmcnt(7)
	v_mfma_f32_32x32x16_f16 v[66:81], v[112:115], v[182:185], v[66:81]
	s_waitcnt lgkmcnt(6)
	s_add_i32 m0, s11, 0xa000
	v_mfma_f32_32x32x16_f16 v[34:49], v[138:141], v[186:189], v[34:49]
	global_load_lds_dwordx4 v[178:179], off
	v_lshl_add_u64 v[178:179], v[178:179], 0, s[2:3]
	v_mfma_f32_32x32x16_f16 v[18:33], v[112:115], v[186:189], v[18:33]
	s_waitcnt lgkmcnt(5)
	s_add_i32 m0, s11, 0xc000
	v_mfma_f32_32x32x16_f16 v[50:65], v[116:119], v[182:185], v[50:65]
	global_load_lds_dwordx4 v[180:181], off
	v_lshl_add_u64 v[180:181], v[180:181], 0, s[2:3]
	v_mfma_f32_32x32x16_f16 v[2:17], v[116:119], v[186:189], v[2:17]
	v_add_u32_e32 v146, v142, v125
	v_add_u32_e32 v147, v143, v125
	ds_read_b128 v[182:185], v147
	ds_read_b128 v[138:141], v146 offset:32768
	ds_read_b128 v[112:115], v146 offset:36864
	ds_read_b128 v[186:189], v147 offset:4096
	ds_read_b128 v[116:119], v146 offset:40960
	s_waitcnt lgkmcnt(8)
	v_mfma_f32_32x32x16_f16 v[82:97], v[104:107], v[130:133], v[82:97]
	s_waitcnt lgkmcnt(7)
	v_mfma_f32_32x32x16_f16 v[66:81], v[108:111], v[130:133], v[66:81]
	s_waitcnt lgkmcnt(6)
	v_mfma_f32_32x32x16_f16 v[34:49], v[104:107], v[134:137], v[34:49]
	v_mfma_f32_32x32x16_f16 v[18:33], v[108:111], v[134:137], v[18:33]
	s_waitcnt lgkmcnt(5)
	v_mfma_f32_32x32x16_f16 v[50:65], v[126:129], v[130:133], v[50:65]
	v_mfma_f32_32x32x16_f16 v[2:17], v[126:129], v[134:137], v[2:17]
	s_waitcnt lgkmcnt(3)
	v_mfma_f32_32x32x16_f16 v[82:97], v[138:141], v[182:185], v[82:97]
	s_waitcnt lgkmcnt(2)
	v_mfma_f32_32x32x16_f16 v[66:81], v[112:115], v[182:185], v[66:81]
	s_waitcnt lgkmcnt(1)
	v_mfma_f32_32x32x16_f16 v[34:49], v[138:141], v[186:189], v[34:49]
	v_mfma_f32_32x32x16_f16 v[18:33], v[112:115], v[186:189], v[18:33]
	s_waitcnt lgkmcnt(0)
	v_mfma_f32_32x32x16_f16 v[50:65], v[116:119], v[182:185], v[50:65]
	v_mfma_f32_32x32x16_f16 v[2:17], v[116:119], v[186:189], v[2:17]
	s_add_i32 s9, s9, 1
	s_cmp_lt_i32 s9, s25
	s_cbranch_scc1 .Lqkv_aloop
	s_waitcnt vmcnt(0)
	s_barrier
	s_mul_i32 s10, s23, 0xe000
	v_add_u32_e32 v142, s10, v122
	v_add_u32_e32 v143, s10, v121
	s_xor_b32 s23, s23, 1
	s_xor_b32 s21, s21, 1
	v_add_u32_e32 v144, v142, v120
	v_add_u32_e32 v145, v143, v120
	ds_read_b128 v[130:133], v145
	ds_read_b128 v[104:107], v144 offset:32768
	ds_read_b128 v[108:111], v144 offset:36864
	ds_read_b128 v[134:137], v145 offset:4096
	ds_read_b128 v[126:129], v144 offset:40960
	v_add_u32_e32 v146, v142, v123
	v_add_u32_e32 v147, v143, v123
	ds_read_b128 v[182:185], v147
	ds_read_b128 v[138:141], v146 offset:32768
	ds_read_b128 v[112:115], v146 offset:36864
	ds_read_b128 v[186:189], v147 offset:4096
	ds_read_b128 v[116:119], v146 offset:40960
	s_waitcnt lgkmcnt(8)
	v_mfma_f32_32x32x16_f16 v[82:97], v[104:107], v[130:133], v[82:97]
	s_waitcnt lgkmcnt(7)
	v_mfma_f32_32x32x16_f16 v[66:81], v[108:111], v[130:133], v[66:81]
	s_waitcnt lgkmcnt(6)
	v_mfma_f32_32x32x16_f16 v[34:49], v[104:107], v[134:137], v[34:49]
	v_mfma_f32_32x32x16_f16 v[18:33], v[108:111], v[134:137], v[18:33]
	s_waitcnt lgkmcnt(5)
	v_mfma_f32_32x32x16_f16 v[50:65], v[126:129], v[130:133], v[50:65]
	v_mfma_f32_32x32x16_f16 v[2:17], v[126:129], v[134:137], v[2:17]
	v_add_u32_e32 v144, v142, v124
	v_add_u32_e32 v145, v143, v124
	ds_read_b128 v[130:133], v145
	ds_read_b128 v[104:107], v144 offset:32768
	ds_read_b128 v[108:111], v144 offset:36864
	ds_read_b128 v[134:137], v145 offset:4096
	ds_read_b128 v[126:129], v144 offset:40960
	s_waitcnt lgkmcnt(8)
	v_mfma_f32_32x32x16_f16 v[82:97], v[138:141], v[182:185], v[82:97]
	s_waitcnt lgkmcnt(7)
	v_mfma_f32_32x32x16_f16 v[66:81], v[112:115], v[182:185], v[66:81]
	s_waitcnt lgkmcnt(6)
	v_mfma_f32_32x32x16_f16 v[34:49], v[138:141], v[186:189], v[34:49]
	v_mfma_f32_32x32x16_f16 v[18:33], v[112:115], v[186:189], v[18:33]
	s_waitcnt lgkmcnt(5)
	v_mfma_f32_32x32x16_f16 v[50:65], v[116:119], v[182:185], v[50:65]
	v_mfma_f32_32x32x16_f16 v[2:17], v[116:119], v[186:189], v[2:17]
	v_add_u32_e32 v146, v142, v125
	v_add_u32_e32 v147, v143, v125
	ds_read_b128 v[182:185], v147
	ds_read_b128 v[138:141], v146 offset:32768
	ds_read_b128 v[112:115], v146 offset:36864
	ds_read_b128 v[186:189], v147 offset:4096
	ds_read_b128 v[116:119], v146 offset:40960
	s_waitcnt lgkmcnt(8)
	v_mfma_f32_32x32x16_f16 v[82:97], v[104:107], v[130:133], v[82:97]
	s_waitcnt lgkmcnt(7)
	v_mfma_f32_32x32x16_f16 v[66:81], v[108:111], v[130:133], v[66:81]
	s_waitcnt lgkmcnt(6)
	v_mfma_f32_32x32x16_f16 v[34:49], v[104:107], v[134:137], v[34:49]
	v_mfma_f32_32x32x16_f16 v[18:33], v[108:111], v[134:137], v[18:33]
	s_waitcnt lgkmcnt(5)
	v_mfma_f32_32x32x16_f16 v[50:65], v[126:129], v[130:133], v[50:65]
	v_mfma_f32_32x32x16_f16 v[2:17], v[126:129], v[134:137], v[2:17]
	s_waitcnt lgkmcnt(3)
	v_mfma_f32_32x32x16_f16 v[82:97], v[138:141], v[182:185], v[82:97]
	s_waitcnt lgkmcnt(2)
	v_mfma_f32_32x32x16_f16 v[66:81], v[112:115], v[182:185], v[66:81]
	s_waitcnt lgkmcnt(1)
	v_mfma_f32_32x32x16_f16 v[34:49], v[138:141], v[186:189], v[34:49]
	v_mfma_f32_32x32x16_f16 v[18:33], v[112:115], v[186:189], v[18:33]
	s_waitcnt lgkmcnt(0)
	v_mfma_f32_32x32x16_f16 v[50:65], v[116:119], v[182:185], v[50:65]
	v_mfma_f32_32x32x16_f16 v[2:17], v[116:119], v[186:189], v[2:17]

.LBB2_32:
	s_mov_b32 s8, 0x15555556
	v_mul_hi_u32 v67, v163, s8
	v_cvt_pk_f16_f32 v51, v64, v65
	v_cvt_pk_f16_f32 v50, v62, v63
	ds_write_b64 v1, v[50:51] offset:176
	v_mul_u32_u24_e32 v50, 12, v67
	v_sub_u32_e32 v50, v163, v50
	v_lshl_add_u32 v60, v50, 3, s12
	v_mul_u32_u24_e32 v51, 0xd0, v67
	v_lshlrev_b32_e32 v76, 4, v50
	v_ashrrev_i32_e32 v52, 6, v60
	v_add3_u32 v51, s11, v51, v76
	v_or_b32_e32 v50, s10, v67
	v_ashrrev_i32_e32 v53, 31, v52
	ds_read_b128 v[54:57], v51
	v_ashrrev_i32_e32 v51, 31, v50
	v_lshlrev_b64 v[52:53], 19, v[52:53]
	s_waitcnt lgkmcnt(0)
	v_lshl_add_u64 v[52:53], s[6:7], 0, v[52:53]
	v_lshlrev_b64 v[50:51], 7, v[50:51]
	v_lshl_add_u64 v[58:59], v[52:53], 0, v[50:51]
	v_and_b32_e32 v50, 56, v60
	v_mov_b32_e32 v51, 0
	v_lshlrev_b32_e32 v50, 1, v50
	v_lshl_add_u64 v[62:63], v[58:59], 0, v[50:51]
	v_or_b32_e32 v58, 64, v163
	v_mul_hi_u32 v77, v58, s8
	v_mul_u32_u24_e32 v59, 12, v77
	v_sub_u32_e32 v64, v58, v59
	v_lshlrev_b32_e32 v78, 4, v64
	v_lshl_add_u32 v64, v64, 3, s12
	global_store_dwordx4 v[62:63], v[54:57], off sc1
	v_mul_u32_u24_e32 v58, 0xd0, v77
	v_add3_u32 v58, s11, v58, v78
	v_ashrrev_i32_e32 v54, 6, v64
	v_or_b32_e32 v56, s10, v77
	v_ashrrev_i32_e32 v55, 31, v54
	v_ashrrev_i32_e32 v57, 31, v56
	v_lshlrev_b64 v[54:55], 19, v[54:55]
	ds_read_b128 v[58:61], v58
	v_lshl_add_u64 v[54:55], s[6:7], 0, v[54:55]
	v_lshlrev_b64 v[56:57], 7, v[56:57]
	v_lshl_add_u64 v[62:63], v[54:55], 0, v[56:57]
	v_and_b32_e32 v56, 56, v64
	v_lshlrev_b32_e32 v56, 1, v56
	v_mov_b32_e32 v57, v51
	v_lshl_add_u64 v[62:63], v[62:63], 0, v[56:57]
	v_or_b32_e32 v57, 0x80, v163
	v_mul_hi_u32 v79, v57, s8
	s_waitcnt lgkmcnt(0)
	global_store_dwordx4 v[62:63], v[58:61], off sc1
	s_and_b64 vcc, exec, s[0:1]
	s_nop 0
	v_mul_u32_u24_e32 v58, 12, v79
	v_sub_u32_e32 v57, v57, v58
	v_mul_u32_u24_e32 v58, 0xd0, v79
	v_lshlrev_b32_e32 v80, 4, v57
	v_add3_u32 v58, s11, v58, v80
	v_lshl_add_u32 v57, v57, 3, s12
	ds_read_b128 v[62:65], v58
	v_ashrrev_i32_e32 v58, 6, v57
	v_or_b32_e32 v60, s10, v79
	v_ashrrev_i32_e32 v59, 31, v58
	v_ashrrev_i32_e32 v61, 31, v60
	v_lshlrev_b64 v[58:59], 19, v[58:59]
	v_lshl_add_u64 v[58:59], s[6:7], 0, v[58:59]
	v_lshlrev_b64 v[60:61], 7, v[60:61]
	v_and_b32_e32 v57, 56, v57
	v_lshl_add_u64 v[68:69], v[58:59], 0, v[60:61]
	v_lshlrev_b32_e32 v60, 1, v57
	v_or_b32_e32 v57, 0xc0, v163
	v_mov_b32_e32 v61, v51
	v_mul_hi_u32 v81, v57, s8
	v_lshl_add_u64 v[72:73], v[68:69], 0, v[60:61]
	v_mul_u32_u24_e32 v61, 12, v81
	v_sub_u32_e32 v57, v57, v61
	v_lshlrev_b32_e32 v83, 4, v57
	v_lshl_add_u32 v57, v57, 3, s12
	s_waitcnt lgkmcnt(0)
	global_store_dwordx4 v[72:73], v[62:65], off sc1
	v_mul_u32_u24_e32 v61, 0xd0, v81
	v_add3_u32 v61, s11, v61, v83
	v_ashrrev_i32_e32 v62, 6, v57
	v_or_b32_e32 v64, s10, v81
	v_ashrrev_i32_e32 v63, 31, v62
	v_ashrrev_i32_e32 v65, 31, v64
	v_lshlrev_b64 v[62:63], 19, v[62:63]
	v_lshl_add_u64 v[62:63], s[6:7], 0, v[62:63]
	v_lshlrev_b64 v[64:65], 7, v[64:65]
	v_and_b32_e32 v57, 56, v57
	ds_read_b128 v[68:71], v61
	v_lshl_add_u64 v[72:73], v[62:63], 0, v[64:65]
	v_lshlrev_b32_e32 v64, 1, v57
	v_or_b32_e32 v57, 0x100, v163
	v_mul_hi_u32 v84, v57, s8
	v_mul_u32_u24_e32 v61, 12, v84
	v_mov_b32_e32 v65, v51
	v_sub_u32_e32 v57, v57, v61
	v_lshl_add_u64 v[72:73], v[72:73], 0, v[64:65]
	v_lshlrev_b32_e32 v85, 4, v57
	v_lshl_add_u32 v57, v57, 3, s12
	s_waitcnt lgkmcnt(0)
	global_store_dwordx4 v[72:73], v[68:71], off sc1
	v_mul_u32_u24_e32 v61, 0xd0, v84
	v_add3_u32 v61, s11, v61, v85
	v_ashrrev_i32_e32 v68, 6, v57
	v_or_b32_e32 v70, s10, v84
	v_ashrrev_i32_e32 v69, 31, v68
	v_ashrrev_i32_e32 v71, 31, v70
	v_lshlrev_b64 v[68:69], 19, v[68:69]
	v_lshl_add_u64 v[68:69], s[6:7], 0, v[68:69]
	v_lshlrev_b64 v[70:71], 7, v[70:71]
	v_and_b32_e32 v57, 56, v57
	ds_read_b128 v[72:75], v61
	v_lshl_add_u64 v[86:87], v[68:69], 0, v[70:71]
	v_lshlrev_b32_e32 v70, 1, v57
	v_mov_b32_e32 v71, v51
	v_or_b32_e32 v57, 0x140, v163
	v_lshl_add_u64 v[92:93], v[86:87], 0, v[70:71]
	v_mul_hi_u32 v86, v57, s8
	v_mul_u32_u24_e32 v61, 12, v86
	v_sub_u32_e32 v57, v57, v61
	v_mul_u32_u24_e32 v61, 0xd0, v86
	v_lshlrev_b32_e32 v87, 4, v57
	v_lshl_add_u32 v57, v57, 3, s12
	v_add3_u32 v61, s11, v61, v87
	s_waitcnt lgkmcnt(0)
	global_store_dwordx4 v[92:93], v[72:75], off sc1
	ds_read_b128 v[88:91], v61
	s_nop 0
	v_ashrrev_i32_e32 v72, 6, v57
	v_or_b32_e32 v74, s10, v86
	v_ashrrev_i32_e32 v73, 31, v72
	v_ashrrev_i32_e32 v75, 31, v74
	v_lshlrev_b64 v[72:73], 19, v[72:73]
	v_lshl_add_u64 v[72:73], s[6:7], 0, v[72:73]
	v_lshlrev_b64 v[74:75], 7, v[74:75]
	v_and_b32_e32 v57, 56, v57
	v_lshl_add_u64 v[92:93], v[72:73], 0, v[74:75]
	v_lshlrev_b32_e32 v74, 1, v57
	v_mov_b32_e32 v75, v51
	v_lshl_add_u64 v[92:93], v[92:93], 0, v[74:75]
	s_waitcnt lgkmcnt(0)
	global_store_dwordx4 v[92:93], v[88:91], off sc1
	s_cbranch_vccnz .LBB2_34
	s_waitcnt vmcnt(13)
	v_pk_mul_f32 v[88:89], v[34:35], v[110:111] op_sel:[1,1] op_sel_hi:[0,1]
	v_pk_fma_f32 v[90:91], v[34:35], v[110:111], v[88:89] neg_lo:[0,0,1] neg_hi:[0,0,1]
	v_pk_fma_f32 v[34:35], v[34:35], v[110:111], v[88:89] op_sel_hi:[1,0,1]
	s_nop 0
	v_mov_b32_e32 v91, v35
	v_pk_mul_f32 v[34:35], v[36:37], v[112:113] op_sel:[1,1] op_sel_hi:[0,1]
	v_pk_fma_f32 v[88:89], v[36:37], v[112:113], v[34:35] neg_lo:[0,0,1] neg_hi:[0,0,1]
	v_pk_fma_f32 v[34:35], v[36:37], v[112:113], v[34:35] op_sel_hi:[1,0,1]
	s_nop 0
	v_mov_b32_e32 v89, v35
	v_pk_mul_f32 v[34:35], v[0:1], v[90:91] op_sel_hi:[0,1]
	v_pk_mul_f32 v[36:37], v[0:1], v[88:89] op_sel_hi:[0,1]

.LBB2_56:
	v_or_b32_e32 v4, 32, v67
	v_cvt_pk_f16_f32 v3, v16, v17
	v_cvt_pk_f16_f32 v2, v14, v15
	v_mul_u32_u24_e32 v0, 0xd0, v4
	ds_write_b64 v1, v[2:3] offset:6832
	v_add3_u32 v0, s11, v0, v76
	v_or_b32_e32 v4, s10, v4
	ds_read_b128 v[0:3], v0
	v_ashrrev_i32_e32 v5, 31, v4
	v_lshlrev_b64 v[4:5], 7, v[4:5]
	v_lshl_add_u64 v[4:5], v[52:53], 0, v[4:5]
	v_mov_b32_e32 v51, 0
	v_or_b32_e32 v10, 32, v77
	v_lshl_add_u64 v[8:9], v[4:5], 0, v[50:51]
	v_mul_u32_u24_e32 v4, 0xd0, v10
	v_add3_u32 v4, s11, v4, v78
	ds_read_b128 v[4:7], v4
	s_waitcnt lgkmcnt(1)
	global_store_dwordx4 v[8:9], v[0:3], off sc1
	v_mov_b32_e32 v57, v51
	v_mov_b32_e32 v61, v51
	v_or_b32_e32 v0, s10, v10
	v_ashrrev_i32_e32 v1, 31, v0
	v_lshlrev_b64 v[0:1], 7, v[0:1]
	v_lshl_add_u64 v[0:1], v[54:55], 0, v[0:1]
	v_lshl_add_u64 v[0:1], v[0:1], 0, v[56:57]
	s_waitcnt lgkmcnt(0)
	global_store_dwordx4 v[0:1], v[4:7], off sc1
	v_or_b32_e32 v10, 32, v81
	v_mov_b32_e32 v65, v51
	v_or_b32_e32 v4, 32, v79
	v_mul_u32_u24_e32 v0, 0xd0, v4
	v_add3_u32 v0, s11, v0, v80
	v_or_b32_e32 v4, s10, v4
	ds_read_b128 v[0:3], v0
	v_ashrrev_i32_e32 v5, 31, v4
	v_lshlrev_b64 v[4:5], 7, v[4:5]
	v_lshl_add_u64 v[4:5], v[58:59], 0, v[4:5]
	v_lshl_add_u64 v[8:9], v[4:5], 0, v[60:61]
	v_mul_u32_u24_e32 v4, 0xd0, v10
	v_add3_u32 v4, s11, v4, v83
	ds_read_b128 v[4:7], v4
	s_waitcnt lgkmcnt(1)
	global_store_dwordx4 v[8:9], v[0:3], off sc1
	v_mov_b32_e32 v71, v51
	v_mov_b32_e32 v75, v51
	v_or_b32_e32 v0, s10, v10
	v_ashrrev_i32_e32 v1, 31, v0
	v_lshlrev_b64 v[0:1], 7, v[0:1]
	v_lshl_add_u64 v[0:1], v[62:63], 0, v[0:1]
	v_lshl_add_u64 v[0:1], v[0:1], 0, v[64:65]
	s_waitcnt lgkmcnt(0)
	global_store_dwordx4 v[0:1], v[4:7], off sc1
	v_or_b32_e32 v10, 32, v86
	s_nop 0
	v_or_b32_e32 v4, 32, v84
	v_mul_u32_u24_e32 v0, 0xd0, v4
	v_add3_u32 v0, s11, v0, v85
	v_or_b32_e32 v4, s10, v4
	ds_read_b128 v[0:3], v0
	v_ashrrev_i32_e32 v5, 31, v4
	v_lshlrev_b64 v[4:5], 7, v[4:5]
	v_lshl_add_u64 v[4:5], v[68:69], 0, v[4:5]
	v_lshl_add_u64 v[8:9], v[4:5], 0, v[70:71]
	v_mul_u32_u24_e32 v4, 0xd0, v10
	v_add3_u32 v4, s11, v4, v87
	ds_read_b128 v[4:7], v4
	s_waitcnt lgkmcnt(1)
	global_store_dwordx4 v[8:9], v[0:3], off sc1
	s_nop 1
	v_or_b32_e32 v0, s10, v10
	v_ashrrev_i32_e32 v1, 31, v0
	v_lshlrev_b64 v[0:1], 7, v[0:1]
	v_lshl_add_u64 v[0:1], v[72:73], 0, v[0:1]
	v_lshl_add_u64 v[0:1], v[0:1], 0, v[74:75]
	s_waitcnt lgkmcnt(0)
	global_store_dwordx4 v[0:1], v[4:7], off sc1
	s_endpgm
	.p2align	8
